# PEER gather V pass: row byte offsets precomputed per token, four readlanes then eight loads per batch (on top of v43)
# speedup vs baseline: 1.0112x; 1.0040x over previous
.LBB0_1138:
	v_and_b32_e32 v4, 15, v148
	v_cmp_eq_u32_e32 vcc, 0, v4
	v_lshlrev_b32_e32 v5, 5, v40
	v_add_u32_e32 v10, 0x80, v148
	v_cndmask_b32_e32 v10, v10, v5, vcc
	v_cmp_gt_u32_e64 s[6:7], 8, v4
	v_lshl_add_u32 v32, v10, 2, v111
	v_and_b32_e32 v36, 12, v148
	v_cndmask_b32_e64 v10, 0, v252, s[6:7]
	v_cmp_lt_u32_e64 s[6:7], 3, v4
	v_lshl_or_b32 v4, v41, 3, v5
	v_add_u32_e32 v34, 0x400, v4
	v_lshlrev_b32_e32 v4, 4, v41
	v_lshl_or_b32 v35, v40, 6, v4
	ds_bpermute_b32 v4, v36, v130
	v_cmp_eq_u32_e32 vcc, 3, v41
	v_cmp_eq_u32_e64 s[2:3], 2, v41
	v_cmp_eq_u32_e64 s[4:5], 1, v41
	v_lshlrev_b32_e32 v129, 4, v148
	s_waitcnt lgkmcnt(0)
	v_mul_lo_u32 v4, v4, s43
	v_add_u32_e32 v5, v4, v35
	v_add_u32_e32 v4, v4, v34
	buffer_load_dwordx4 v[38:41], v5, s[44:47], 0 offen
	buffer_load_dwordx2 v[42:43], v4, s[44:47], 0 offen
	buffer_load_dwordx4 v[44:47], v5, s[44:47], s21 offen
	buffer_load_dwordx2 v[48:49], v4, s[44:47], s33 offen
	buffer_load_dwordx4 v[50:53], v5, s[44:47], s20 offen
	buffer_load_dwordx2 v[54:55], v4, s[44:47], s21 offen
	buffer_load_dwordx4 v[56:59], v5, s[44:47], s23 offen
	buffer_load_dwordx2 v[60:61], v4, s[44:47], s94 offen
	s_mov_b32 s0, 0
	v_cndmask_b32_e64 v33, 1.0, v10, s[6:7]
	ds_bpermute_b32 v4, v36, v130 offset:16
	s_waitcnt lgkmcnt(0)
	v_mul_lo_u32 v4, v4, s43
	v_add_u32_e32 v5, v4, v35
	v_add_u32_e32 v4, v4, v34
	buffer_load_dwordx4 v[62:65], v5, s[44:47], 0 offen
	buffer_load_dwordx4 v[68:71], v5, s[44:47], s20 offen
	buffer_load_dwordx4 v[74:77], v5, s[44:47], s21 offen
	buffer_load_dwordx4 v[86:89], v5, s[44:47], s23 offen
	buffer_load_dwordx2 v[66:67], v4, s[44:47], 0 offen
	buffer_load_dwordx2 v[78:79], v4, s[44:47], s33 offen
	buffer_load_dwordx2 v[72:73], v4, s[44:47], s21 offen
	buffer_load_dwordx2 v[90:91], v4, s[44:47], s94 offen
	ds_bpermute_b32 v4, v36, v130 offset:32
	s_waitcnt lgkmcnt(0)
	v_mul_lo_u32 v4, v4, s43
	v_add_u32_e32 v5, v4, v35
	v_add_u32_e32 v4, v4, v34
	buffer_load_dwordx4 v[92:95], v5, s[44:47], 0 offen
	buffer_load_dwordx4 v[98:101], v5, s[44:47], s20 offen
	buffer_load_dwordx4 v[150:153], v5, s[44:47], s21 offen
	buffer_load_dwordx4 v[156:159], v5, s[44:47], s23 offen
	buffer_load_dwordx2 v[96:97], v4, s[44:47], 0 offen
	buffer_load_dwordx2 v[154:155], v4, s[44:47], s33 offen
	buffer_load_dwordx2 v[102:103], v4, s[44:47], s21 offen
	buffer_load_dwordx2 v[160:161], v4, s[44:47], s94 offen
	ds_bpermute_b32 v4, v36, v130 offset:48
	s_waitcnt lgkmcnt(0)
	v_mul_lo_u32 v4, v4, s43
	v_add_u32_e32 v5, v4, v35
	v_add_u32_e32 v4, v4, v34
	buffer_load_dwordx4 v[162:165], v5, s[44:47], 0 offen
	buffer_load_dwordx4 v[168:171], v5, s[44:47], s20 offen
	buffer_load_dwordx4 v[174:177], v5, s[44:47], s21 offen
	buffer_load_dwordx4 v[216:219], v5, s[44:47], s23 offen
	buffer_load_dwordx2 v[166:167], v4, s[44:47], 0 offen
	buffer_load_dwordx2 v[178:179], v4, s[44:47], s33 offen
	buffer_load_dwordx2 v[172:173], v4, s[44:47], s21 offen
	buffer_load_dwordx2 v[220:221], v4, s[44:47], s94 offen
	v_mov_b32_e32 v22, v28
	v_mov_b32_e32 v23, v29
	v_mov_b32_e32 v16, v30
	v_mov_b32_e32 v17, v31
	s_waitcnt vmcnt(30)
	v_mfma_f32_16x16x128_f8f6f4 v[38:41], v[38:43], v[18:23], 0 cbsz:2 blgp:2
	v_mov_b32_e32 v10, v24
	v_mov_b32_e32 v11, v25
	v_mov_b32_e32 v4, v26
	s_waitcnt vmcnt(28)
	v_mfma_f32_16x16x128_f8f6f4 v[28:31], v[44:49], v[12:17], v[38:41] cbsz:2 blgp:2
	v_mov_b32_e32 v5, v27
	s_waitcnt vmcnt(26)
	v_mfma_f32_16x16x128_f8f6f4 v[28:31], v[50:55], v[6:11], v[28:31] cbsz:2 blgp:2
	s_waitcnt vmcnt(24)
	v_mfma_f32_16x16x128_f8f6f4 v[24:27], v[56:61], v[0:5], v[28:31] cbsz:2 blgp:2
	s_nop 7
	v_cndmask_b32_e64 v24, v24, v25, s[4:5]
	v_cndmask_b32_e64 v24, v24, v26, s[2:3]
	v_cndmask_b32_e32 v24, v24, v27, vcc
	v_mul_f32_e32 v25, v33, v24
	s_nop 1
	v_mov_b32_dpp v25, v25 quad_perm:[1,0,3,2] row_mask:0xf bank_mask:0xf bound_ctrl:1
	v_fmac_f32_e32 v25, v33, v24
	s_nop 1
	v_add_f32_dpp v24, v25, v25 quad_perm:[2,3,0,1] row_mask:0xf bank_mask:0xf bound_ctrl:1
	s_nop 1
	v_add_f32_dpp v24, v24, v24 row_half_mirror row_mask:0xf bank_mask:0xf bound_ctrl:1
	ds_write_b32 v32, v24 offset:49152
	ds_bpermute_b32 v24, v36, v130 offset:64
	s_waitcnt lgkmcnt(0)
	v_mul_lo_u32 v24, v24, s43
	v_add_u32_e32 v28, v24, v35
	v_add_u32_e32 v30, v24, v34
	buffer_load_dwordx4 v[24:27], v28, s[44:47], 0 offen
	buffer_load_dwordx4 v[38:41], v28, s[44:47], s20 offen
	buffer_load_dwordx4 v[44:47], v28, s[44:47], s21 offen
	buffer_load_dwordx4 v[50:53], v28, s[44:47], s23 offen
	s_nop 0
	buffer_load_dwordx2 v[28:29], v30, s[44:47], 0 offen
	buffer_load_dwordx2 v[48:49], v30, s[44:47], s33 offen
	buffer_load_dwordx2 v[42:43], v30, s[44:47], s21 offen
	buffer_load_dwordx2 v[54:55], v30, s[44:47], s94 offen
	s_waitcnt vmcnt(27)
	v_mfma_f32_16x16x128_f8f6f4 v[56:59], v[62:67], v[18:23], 0 cbsz:2 blgp:2
	s_waitcnt vmcnt(26)
	v_mfma_f32_16x16x128_f8f6f4 v[56:59], v[74:79], v[12:17], v[56:59] cbsz:2 blgp:2
	s_waitcnt vmcnt(25)
	v_mfma_f32_16x16x128_f8f6f4 v[56:59], v[68:73], v[6:11], v[56:59] cbsz:2 blgp:2
	s_waitcnt vmcnt(24)
	v_mfma_f32_16x16x128_f8f6f4 v[56:59], v[86:91], v[0:5], v[56:59] cbsz:2 blgp:2
	s_nop 7
	v_cndmask_b32_e64 v30, v56, v57, s[4:5]
	v_cndmask_b32_e64 v30, v30, v58, s[2:3]
	v_cndmask_b32_e32 v30, v30, v59, vcc
	v_mul_f32_e32 v31, v33, v30
	s_nop 1
	v_mov_b32_dpp v31, v31 quad_perm:[1,0,3,2] row_mask:0xf bank_mask:0xf bound_ctrl:1
	v_fmac_f32_e32 v31, v33, v30
	s_nop 1
	v_add_f32_dpp v30, v31, v31 quad_perm:[2,3,0,1] row_mask:0xf bank_mask:0xf bound_ctrl:1
	s_nop 1
	v_add_f32_dpp v30, v30, v30 row_half_mirror row_mask:0xf bank_mask:0xf bound_ctrl:1
	ds_write_b32 v32, v30 offset:49156
	ds_bpermute_b32 v30, v36, v130 offset:80
	s_waitcnt lgkmcnt(0)
	v_mul_lo_u32 v30, v30, s43
	v_add_u32_e32 v31, v30, v35
	v_add_u32_e32 v30, v30, v34
	buffer_load_dwordx4 v[56:59], v31, s[44:47], 0 offen
	buffer_load_dwordx4 v[62:65], v31, s[44:47], s20 offen
	buffer_load_dwordx4 v[68:71], v31, s[44:47], s21 offen
	buffer_load_dwordx4 v[74:77], v31, s[44:47], s23 offen
	buffer_load_dwordx2 v[60:61], v30, s[44:47], 0 offen
	buffer_load_dwordx2 v[72:73], v30, s[44:47], s33 offen
	buffer_load_dwordx2 v[66:67], v30, s[44:47], s21 offen
	buffer_load_dwordx2 v[78:79], v30, s[44:47], s94 offen
	s_waitcnt vmcnt(27)
	v_mfma_f32_16x16x128_f8f6f4 v[86:89], v[92:97], v[18:23], 0 cbsz:2 blgp:2
	s_waitcnt vmcnt(26)
	v_mfma_f32_16x16x128_f8f6f4 v[86:89], v[150:155], v[12:17], v[86:89] cbsz:2 blgp:2
	s_waitcnt vmcnt(25)
	v_mfma_f32_16x16x128_f8f6f4 v[86:89], v[98:103], v[6:11], v[86:89] cbsz:2 blgp:2
	s_waitcnt vmcnt(24)
	v_mfma_f32_16x16x128_f8f6f4 v[86:89], v[156:161], v[0:5], v[86:89] cbsz:2 blgp:2
	s_nop 7
	v_cndmask_b32_e64 v30, v86, v87, s[4:5]
	v_cndmask_b32_e64 v30, v30, v88, s[2:3]
	v_cndmask_b32_e32 v30, v30, v89, vcc
	v_mul_f32_e32 v31, v33, v30
	s_nop 1
	v_mov_b32_dpp v31, v31 quad_perm:[1,0,3,2] row_mask:0xf bank_mask:0xf bound_ctrl:1
	v_fmac_f32_e32 v31, v33, v30
	s_nop 1
	v_add_f32_dpp v30, v31, v31 quad_perm:[2,3,0,1] row_mask:0xf bank_mask:0xf bound_ctrl:1
	s_nop 1
	v_add_f32_dpp v30, v30, v30 row_half_mirror row_mask:0xf bank_mask:0xf bound_ctrl:1
	ds_write_b32 v32, v30 offset:49160
	ds_bpermute_b32 v30, v36, v130 offset:96
	s_waitcnt lgkmcnt(0)
	v_mul_lo_u32 v30, v30, s43
	v_add_u32_e32 v31, v30, v35
	v_add_u32_e32 v30, v30, v34
	buffer_load_dwordx4 v[86:89], v31, s[44:47], 0 offen
	buffer_load_dwordx4 v[92:95], v31, s[44:47], s20 offen
	buffer_load_dwordx4 v[98:101], v31, s[44:47], s21 offen
	buffer_load_dwordx4 v[150:153], v31, s[44:47], s23 offen
	buffer_load_dwordx2 v[90:91], v30, s[44:47], 0 offen
	buffer_load_dwordx2 v[102:103], v30, s[44:47], s33 offen
	buffer_load_dwordx2 v[96:97], v30, s[44:47], s21 offen
	buffer_load_dwordx2 v[154:155], v30, s[44:47], s94 offen
	s_waitcnt vmcnt(27)
	v_mfma_f32_16x16x128_f8f6f4 v[156:159], v[162:167], v[18:23], 0 cbsz:2 blgp:2
	s_waitcnt vmcnt(26)
	v_mfma_f32_16x16x128_f8f6f4 v[156:159], v[174:179], v[12:17], v[156:159] cbsz:2 blgp:2
	s_waitcnt vmcnt(25)
	v_mfma_f32_16x16x128_f8f6f4 v[156:159], v[168:173], v[6:11], v[156:159] cbsz:2 blgp:2
	s_waitcnt vmcnt(24)
	v_mfma_f32_16x16x128_f8f6f4 v[156:159], v[216:221], v[0:5], v[156:159] cbsz:2 blgp:2
	s_nop 7
	v_cndmask_b32_e64 v30, v156, v157, s[4:5]
	v_cndmask_b32_e64 v30, v30, v158, s[2:3]
	v_cndmask_b32_e32 v30, v30, v159, vcc
	v_mul_f32_e32 v31, v33, v30
	s_nop 1
	v_mov_b32_dpp v31, v31 quad_perm:[1,0,3,2] row_mask:0xf bank_mask:0xf bound_ctrl:1
	v_fmac_f32_e32 v31, v33, v30
	s_nop 1
	v_add_f32_dpp v30, v31, v31 quad_perm:[2,3,0,1] row_mask:0xf bank_mask:0xf bound_ctrl:1
	s_nop 1
	v_add_f32_dpp v30, v30, v30 row_half_mirror row_mask:0xf bank_mask:0xf bound_ctrl:1
	ds_write_b32 v32, v30 offset:49164
	ds_bpermute_b32 v30, v36, v130 offset:112
	s_waitcnt lgkmcnt(0)
	v_mul_lo_u32 v30, v30, s43
	v_add_u32_e32 v31, v30, v35
	v_add_u32_e32 v30, v30, v34
	buffer_load_dwordx4 v[156:159], v31, s[44:47], 0 offen
	buffer_load_dwordx4 v[162:165], v31, s[44:47], s20 offen
	buffer_load_dwordx4 v[168:171], v31, s[44:47], s21 offen
	buffer_load_dwordx4 v[174:177], v31, s[44:47], s23 offen
	buffer_load_dwordx2 v[160:161], v30, s[44:47], 0 offen
	buffer_load_dwordx2 v[172:173], v30, s[44:47], s33 offen
	buffer_load_dwordx2 v[166:167], v30, s[44:47], s21 offen
	buffer_load_dwordx2 v[178:179], v30, s[44:47], s94 offen
	s_waitcnt vmcnt(27)
	v_mfma_f32_16x16x128_f8f6f4 v[24:27], v[24:29], v[18:23], 0 cbsz:2 blgp:2
	s_waitcnt vmcnt(26)
	v_mfma_f32_16x16x128_f8f6f4 v[24:27], v[44:49], v[12:17], v[24:27] cbsz:2 blgp:2
	s_waitcnt vmcnt(25)
	v_mfma_f32_16x16x128_f8f6f4 v[24:27], v[38:43], v[6:11], v[24:27] cbsz:2 blgp:2
	s_waitcnt vmcnt(24)
	v_mfma_f32_16x16x128_f8f6f4 v[24:27], v[50:55], v[0:5], v[24:27] cbsz:2 blgp:2
	s_nop 7
	v_cndmask_b32_e64 v24, v24, v25, s[4:5]
	v_cndmask_b32_e64 v24, v24, v26, s[2:3]
	v_cndmask_b32_e32 v24, v24, v27, vcc
	v_mul_f32_e32 v25, v33, v24
	s_nop 1
	v_mov_b32_dpp v25, v25 quad_perm:[1,0,3,2] row_mask:0xf bank_mask:0xf bound_ctrl:1
	v_fmac_f32_e32 v25, v33, v24
	s_nop 1
	v_add_f32_dpp v24, v25, v25 quad_perm:[2,3,0,1] row_mask:0xf bank_mask:0xf bound_ctrl:1
	s_nop 1
	v_add_f32_dpp v24, v24, v24 row_half_mirror row_mask:0xf bank_mask:0xf bound_ctrl:1
	ds_write_b32 v32, v24 offset:49168
	ds_bpermute_b32 v24, v36, v130 offset:128
	s_waitcnt lgkmcnt(0)
	v_mul_lo_u32 v24, v24, s43
	v_add_u32_e32 v28, v24, v35
	v_add_u32_e32 v30, v24, v34
	buffer_load_dwordx4 v[24:27], v28, s[44:47], 0 offen
	buffer_load_dwordx4 v[38:41], v28, s[44:47], s20 offen
	buffer_load_dwordx4 v[44:47], v28, s[44:47], s21 offen
	buffer_load_dwordx4 v[50:53], v28, s[44:47], s23 offen
	s_nop 0
	buffer_load_dwordx2 v[28:29], v30, s[44:47], 0 offen
	buffer_load_dwordx2 v[48:49], v30, s[44:47], s33 offen
	buffer_load_dwordx2 v[42:43], v30, s[44:47], s21 offen
	buffer_load_dwordx2 v[54:55], v30, s[44:47], s94 offen
	s_waitcnt vmcnt(27)
	v_mfma_f32_16x16x128_f8f6f4 v[56:59], v[56:61], v[18:23], 0 cbsz:2 blgp:2
	s_waitcnt vmcnt(26)
	v_mfma_f32_16x16x128_f8f6f4 v[56:59], v[68:73], v[12:17], v[56:59] cbsz:2 blgp:2
	s_waitcnt vmcnt(25)
	v_mfma_f32_16x16x128_f8f6f4 v[56:59], v[62:67], v[6:11], v[56:59] cbsz:2 blgp:2
	s_waitcnt vmcnt(24)
	v_mfma_f32_16x16x128_f8f6f4 v[56:59], v[74:79], v[0:5], v[56:59] cbsz:2 blgp:2
	s_nop 7
	v_cndmask_b32_e64 v30, v56, v57, s[4:5]
	v_cndmask_b32_e64 v30, v30, v58, s[2:3]
	v_cndmask_b32_e32 v30, v30, v59, vcc
	v_mul_f32_e32 v31, v33, v30
	s_nop 1
	v_mov_b32_dpp v31, v31 quad_perm:[1,0,3,2] row_mask:0xf bank_mask:0xf bound_ctrl:1
	v_fmac_f32_e32 v31, v33, v30
	s_nop 1
	v_add_f32_dpp v30, v31, v31 quad_perm:[2,3,0,1] row_mask:0xf bank_mask:0xf bound_ctrl:1
	s_nop 1
	v_add_f32_dpp v30, v30, v30 row_half_mirror row_mask:0xf bank_mask:0xf bound_ctrl:1
	ds_write_b32 v32, v30 offset:49172
	ds_bpermute_b32 v30, v36, v130 offset:144
	s_waitcnt lgkmcnt(0)
	v_mul_lo_u32 v30, v30, s43
	v_add_u32_e32 v31, v30, v35
	v_add_u32_e32 v30, v30, v34
	buffer_load_dwordx4 v[56:59], v31, s[44:47], 0 offen
	buffer_load_dwordx4 v[62:65], v31, s[44:47], s20 offen
	buffer_load_dwordx4 v[68:71], v31, s[44:47], s21 offen
	buffer_load_dwordx4 v[74:77], v31, s[44:47], s23 offen
	buffer_load_dwordx2 v[60:61], v30, s[44:47], 0 offen
	buffer_load_dwordx2 v[72:73], v30, s[44:47], s33 offen
	buffer_load_dwordx2 v[66:67], v30, s[44:47], s21 offen
	buffer_load_dwordx2 v[78:79], v30, s[44:47], s94 offen
	s_waitcnt vmcnt(27)
	v_mfma_f32_16x16x128_f8f6f4 v[86:89], v[86:91], v[18:23], 0 cbsz:2 blgp:2
	s_waitcnt vmcnt(26)
	v_mfma_f32_16x16x128_f8f6f4 v[86:89], v[98:103], v[12:17], v[86:89] cbsz:2 blgp:2
	s_waitcnt vmcnt(25)
	v_mfma_f32_16x16x128_f8f6f4 v[86:89], v[92:97], v[6:11], v[86:89] cbsz:2 blgp:2
	s_waitcnt vmcnt(24)
	v_mfma_f32_16x16x128_f8f6f4 v[86:89], v[150:155], v[0:5], v[86:89] cbsz:2 blgp:2
	s_nop 7
	v_cndmask_b32_e64 v30, v86, v87, s[4:5]
	v_cndmask_b32_e64 v30, v30, v88, s[2:3]
	v_cndmask_b32_e32 v30, v30, v89, vcc
	v_mul_f32_e32 v31, v33, v30
	s_nop 1
	v_mov_b32_dpp v31, v31 quad_perm:[1,0,3,2] row_mask:0xf bank_mask:0xf bound_ctrl:1
	v_fmac_f32_e32 v31, v33, v30
	s_nop 1
	v_add_f32_dpp v30, v31, v31 quad_perm:[2,3,0,1] row_mask:0xf bank_mask:0xf bound_ctrl:1
	s_nop 1
	v_add_f32_dpp v30, v30, v30 row_half_mirror row_mask:0xf bank_mask:0xf bound_ctrl:1
	ds_write_b32 v32, v30 offset:49176
	ds_bpermute_b32 v30, v36, v130 offset:160
	s_waitcnt lgkmcnt(0)
	v_mul_lo_u32 v30, v30, s43
	v_add_u32_e32 v31, v30, v35
	v_add_u32_e32 v30, v30, v34
	buffer_load_dwordx4 v[86:89], v31, s[44:47], 0 offen
	buffer_load_dwordx4 v[92:95], v31, s[44:47], s20 offen
	buffer_load_dwordx4 v[98:101], v31, s[44:47], s21 offen
	buffer_load_dwordx4 v[150:153], v31, s[44:47], s23 offen
	buffer_load_dwordx2 v[90:91], v30, s[44:47], 0 offen
	buffer_load_dwordx2 v[102:103], v30, s[44:47], s33 offen
	buffer_load_dwordx2 v[96:97], v30, s[44:47], s21 offen
	buffer_load_dwordx2 v[154:155], v30, s[44:47], s94 offen
	s_waitcnt vmcnt(27)
	v_mfma_f32_16x16x128_f8f6f4 v[156:159], v[156:161], v[18:23], 0 cbsz:2 blgp:2
	s_waitcnt vmcnt(26)
	v_mfma_f32_16x16x128_f8f6f4 v[156:159], v[168:173], v[12:17], v[156:159] cbsz:2 blgp:2
	s_waitcnt vmcnt(25)
	v_mfma_f32_16x16x128_f8f6f4 v[156:159], v[162:167], v[6:11], v[156:159] cbsz:2 blgp:2
	s_waitcnt vmcnt(24)
	v_mfma_f32_16x16x128_f8f6f4 v[156:159], v[174:179], v[0:5], v[156:159] cbsz:2 blgp:2
	s_nop 7
	v_cndmask_b32_e64 v30, v156, v157, s[4:5]
	v_cndmask_b32_e64 v30, v30, v158, s[2:3]
	v_cndmask_b32_e32 v30, v30, v159, vcc
	v_mul_f32_e32 v31, v33, v30
	s_nop 1
	v_mov_b32_dpp v31, v31 quad_perm:[1,0,3,2] row_mask:0xf bank_mask:0xf bound_ctrl:1
	v_fmac_f32_e32 v31, v33, v30
	s_nop 1
	v_add_f32_dpp v30, v31, v31 quad_perm:[2,3,0,1] row_mask:0xf bank_mask:0xf bound_ctrl:1
	s_nop 1
	v_add_f32_dpp v30, v30, v30 row_half_mirror row_mask:0xf bank_mask:0xf bound_ctrl:1
	ds_write_b32 v32, v30 offset:49180
	ds_bpermute_b32 v30, v36, v130 offset:176
	s_waitcnt lgkmcnt(0)
	v_mul_lo_u32 v30, v30, s43
	v_add_u32_e32 v31, v30, v35
	v_add_u32_e32 v30, v30, v34
	buffer_load_dwordx4 v[156:159], v31, s[44:47], 0 offen
	buffer_load_dwordx4 v[162:165], v31, s[44:47], s20 offen
	buffer_load_dwordx4 v[168:171], v31, s[44:47], s21 offen
	buffer_load_dwordx4 v[174:177], v31, s[44:47], s23 offen
	buffer_load_dwordx2 v[160:161], v30, s[44:47], 0 offen
	buffer_load_dwordx2 v[172:173], v30, s[44:47], s33 offen
	buffer_load_dwordx2 v[166:167], v30, s[44:47], s21 offen
	buffer_load_dwordx2 v[178:179], v30, s[44:47], s94 offen
	s_waitcnt vmcnt(27)
	v_mfma_f32_16x16x128_f8f6f4 v[24:27], v[24:29], v[18:23], 0 cbsz:2 blgp:2
	s_waitcnt vmcnt(26)
	v_mfma_f32_16x16x128_f8f6f4 v[24:27], v[44:49], v[12:17], v[24:27] cbsz:2 blgp:2
	s_waitcnt vmcnt(25)
	v_mfma_f32_16x16x128_f8f6f4 v[24:27], v[38:43], v[6:11], v[24:27] cbsz:2 blgp:2
	s_waitcnt vmcnt(24)
	v_mfma_f32_16x16x128_f8f6f4 v[24:27], v[50:55], v[0:5], v[24:27] cbsz:2 blgp:2
	s_nop 7
	v_cndmask_b32_e64 v24, v24, v25, s[4:5]
	v_cndmask_b32_e64 v24, v24, v26, s[2:3]
	v_cndmask_b32_e32 v24, v24, v27, vcc
	v_mul_f32_e32 v25, v33, v24
	s_nop 1
	v_mov_b32_dpp v25, v25 quad_perm:[1,0,3,2] row_mask:0xf bank_mask:0xf bound_ctrl:1
	v_fmac_f32_e32 v25, v33, v24
	s_nop 1
	v_add_f32_dpp v24, v25, v25 quad_perm:[2,3,0,1] row_mask:0xf bank_mask:0xf bound_ctrl:1
	s_nop 1
	v_add_f32_dpp v24, v24, v24 row_half_mirror row_mask:0xf bank_mask:0xf bound_ctrl:1
	ds_write_b32 v32, v24 offset:49184
	ds_bpermute_b32 v24, v36, v130 offset:192
	s_waitcnt lgkmcnt(0)
	v_mul_lo_u32 v24, v24, s43
	v_add_u32_e32 v28, v24, v35
	v_add_u32_e32 v30, v24, v34
	buffer_load_dwordx4 v[24:27], v28, s[44:47], 0 offen
	buffer_load_dwordx4 v[38:41], v28, s[44:47], s20 offen
	buffer_load_dwordx4 v[44:47], v28, s[44:47], s21 offen
	buffer_load_dwordx4 v[50:53], v28, s[44:47], s23 offen
	s_nop 0
	buffer_load_dwordx2 v[28:29], v30, s[44:47], 0 offen
	buffer_load_dwordx2 v[48:49], v30, s[44:47], s33 offen
	buffer_load_dwordx2 v[42:43], v30, s[44:47], s21 offen
	buffer_load_dwordx2 v[54:55], v30, s[44:47], s94 offen
	s_waitcnt vmcnt(27)
	v_mfma_f32_16x16x128_f8f6f4 v[56:59], v[56:61], v[18:23], 0 cbsz:2 blgp:2
	s_waitcnt vmcnt(26)
	v_mfma_f32_16x16x128_f8f6f4 v[56:59], v[68:73], v[12:17], v[56:59] cbsz:2 blgp:2
	s_waitcnt vmcnt(25)
	v_mfma_f32_16x16x128_f8f6f4 v[56:59], v[62:67], v[6:11], v[56:59] cbsz:2 blgp:2
	s_waitcnt vmcnt(24)
	v_mfma_f32_16x16x128_f8f6f4 v[56:59], v[74:79], v[0:5], v[56:59] cbsz:2 blgp:2
	s_nop 7
	v_cndmask_b32_e64 v30, v56, v57, s[4:5]
	v_cndmask_b32_e64 v30, v30, v58, s[2:3]
	v_cndmask_b32_e32 v30, v30, v59, vcc
	v_mul_f32_e32 v31, v33, v30
	s_nop 1
	v_mov_b32_dpp v31, v31 quad_perm:[1,0,3,2] row_mask:0xf bank_mask:0xf bound_ctrl:1
	v_fmac_f32_e32 v31, v33, v30
	s_nop 1
	v_add_f32_dpp v30, v31, v31 quad_perm:[2,3,0,1] row_mask:0xf bank_mask:0xf bound_ctrl:1
	s_nop 1
	v_add_f32_dpp v30, v30, v30 row_half_mirror row_mask:0xf bank_mask:0xf bound_ctrl:1
	ds_write_b32 v32, v30 offset:49188
	ds_bpermute_b32 v30, v36, v130 offset:208
	s_waitcnt lgkmcnt(0)
	v_mul_lo_u32 v30, v30, s43
	v_add_u32_e32 v31, v30, v35
	v_add_u32_e32 v30, v30, v34
	buffer_load_dwordx4 v[56:59], v31, s[44:47], 0 offen
	buffer_load_dwordx4 v[62:65], v31, s[44:47], s20 offen
	buffer_load_dwordx4 v[68:71], v31, s[44:47], s21 offen
	buffer_load_dwordx4 v[74:77], v31, s[44:47], s23 offen
	buffer_load_dwordx2 v[60:61], v30, s[44:47], 0 offen
	buffer_load_dwordx2 v[72:73], v30, s[44:47], s33 offen
	buffer_load_dwordx2 v[66:67], v30, s[44:47], s21 offen
	buffer_load_dwordx2 v[78:79], v30, s[44:47], s94 offen
	s_waitcnt vmcnt(27)
	v_mfma_f32_16x16x128_f8f6f4 v[86:89], v[86:91], v[18:23], 0 cbsz:2 blgp:2
	s_waitcnt vmcnt(26)
	v_mfma_f32_16x16x128_f8f6f4 v[86:89], v[98:103], v[12:17], v[86:89] cbsz:2 blgp:2
	s_waitcnt vmcnt(25)
	v_mfma_f32_16x16x128_f8f6f4 v[86:89], v[92:97], v[6:11], v[86:89] cbsz:2 blgp:2
	s_waitcnt vmcnt(24)
	v_mfma_f32_16x16x128_f8f6f4 v[86:89], v[150:155], v[0:5], v[86:89] cbsz:2 blgp:2
	s_nop 7
	v_cndmask_b32_e64 v30, v86, v87, s[4:5]
	v_cndmask_b32_e64 v30, v30, v88, s[2:3]
	v_cndmask_b32_e32 v30, v30, v89, vcc
	v_mul_f32_e32 v31, v33, v30
	s_nop 1
	v_mov_b32_dpp v31, v31 quad_perm:[1,0,3,2] row_mask:0xf bank_mask:0xf bound_ctrl:1
	v_fmac_f32_e32 v31, v33, v30
	s_nop 1
	v_add_f32_dpp v30, v31, v31 quad_perm:[2,3,0,1] row_mask:0xf bank_mask:0xf bound_ctrl:1
	s_nop 1
	v_add_f32_dpp v30, v30, v30 row_half_mirror row_mask:0xf bank_mask:0xf bound_ctrl:1
	ds_write_b32 v32, v30 offset:49192
	ds_bpermute_b32 v30, v36, v130 offset:224
	s_waitcnt lgkmcnt(0)
	v_mul_lo_u32 v30, v30, s43
	v_add_u32_e32 v31, v30, v35
	v_add_u32_e32 v30, v30, v34
	buffer_load_dwordx4 v[86:89], v31, s[44:47], 0 offen
	buffer_load_dwordx4 v[92:95], v31, s[44:47], s20 offen
	buffer_load_dwordx4 v[98:101], v31, s[44:47], s21 offen
	buffer_load_dwordx4 v[150:153], v31, s[44:47], s23 offen
	buffer_load_dwordx2 v[90:91], v30, s[44:47], 0 offen
	buffer_load_dwordx2 v[102:103], v30, s[44:47], s33 offen
	buffer_load_dwordx2 v[96:97], v30, s[44:47], s21 offen
	buffer_load_dwordx2 v[154:155], v30, s[44:47], s94 offen
	s_waitcnt vmcnt(27)
	v_mfma_f32_16x16x128_f8f6f4 v[156:159], v[156:161], v[18:23], 0 cbsz:2 blgp:2
	s_waitcnt vmcnt(26)
	v_mfma_f32_16x16x128_f8f6f4 v[156:159], v[168:173], v[12:17], v[156:159] cbsz:2 blgp:2
	s_waitcnt vmcnt(25)
	v_mfma_f32_16x16x128_f8f6f4 v[156:159], v[162:167], v[6:11], v[156:159] cbsz:2 blgp:2
	s_waitcnt vmcnt(24)
	v_mfma_f32_16x16x128_f8f6f4 v[156:159], v[174:179], v[0:5], v[156:159] cbsz:2 blgp:2
	s_nop 7
	v_cndmask_b32_e64 v30, v156, v157, s[4:5]
	v_cndmask_b32_e64 v30, v30, v158, s[2:3]
	v_cndmask_b32_e32 v30, v30, v159, vcc
	v_mul_f32_e32 v31, v33, v30
	s_nop 1
	v_mov_b32_dpp v31, v31 quad_perm:[1,0,3,2] row_mask:0xf bank_mask:0xf bound_ctrl:1
	v_fmac_f32_e32 v31, v33, v30
	s_nop 1
	v_add_f32_dpp v30, v31, v31 quad_perm:[2,3,0,1] row_mask:0xf bank_mask:0xf bound_ctrl:1
	s_nop 1
	v_add_f32_dpp v30, v30, v30 row_half_mirror row_mask:0xf bank_mask:0xf bound_ctrl:1
	ds_write_b32 v32, v30 offset:49196
	ds_bpermute_b32 v30, v36, v130 offset:240
	s_waitcnt lgkmcnt(0)
	v_mul_lo_u32 v30, v30, s43
	v_add_u32_e32 v31, v30, v35
	v_add_u32_e32 v30, v30, v34
	buffer_load_dwordx4 v[156:159], v31, s[44:47], 0 offen
	buffer_load_dwordx4 v[162:165], v31, s[44:47], s20 offen
	buffer_load_dwordx4 v[168:171], v31, s[44:47], s21 offen
	buffer_load_dwordx4 v[174:177], v31, s[44:47], s23 offen
	buffer_load_dwordx2 v[160:161], v30, s[44:47], 0 offen
	buffer_load_dwordx2 v[172:173], v30, s[44:47], s33 offen
	buffer_load_dwordx2 v[166:167], v30, s[44:47], s21 offen
	buffer_load_dwordx2 v[178:179], v30, s[44:47], s94 offen
	s_waitcnt vmcnt(27)
	v_mfma_f32_16x16x128_f8f6f4 v[24:27], v[24:29], v[18:23], 0 cbsz:2 blgp:2
	s_waitcnt vmcnt(26)
	v_mfma_f32_16x16x128_f8f6f4 v[24:27], v[44:49], v[12:17], v[24:27] cbsz:2 blgp:2
	s_waitcnt vmcnt(25)
	v_mfma_f32_16x16x128_f8f6f4 v[24:27], v[38:43], v[6:11], v[24:27] cbsz:2 blgp:2
	s_waitcnt vmcnt(24)
	v_mfma_f32_16x16x128_f8f6f4 v[24:27], v[50:55], v[0:5], v[24:27] cbsz:2 blgp:2
	s_nop 7
	v_cndmask_b32_e64 v24, v24, v25, s[4:5]
	v_cndmask_b32_e64 v24, v24, v26, s[2:3]
	v_cndmask_b32_e32 v24, v24, v27, vcc
	v_mul_f32_e32 v25, v33, v24
	s_nop 1
	v_mov_b32_dpp v25, v25 quad_perm:[1,0,3,2] row_mask:0xf bank_mask:0xf bound_ctrl:1
	v_fmac_f32_e32 v25, v33, v24
	s_nop 1
	v_add_f32_dpp v24, v25, v25 quad_perm:[2,3,0,1] row_mask:0xf bank_mask:0xf bound_ctrl:1
	s_nop 1
	v_add_f32_dpp v24, v24, v24 row_half_mirror row_mask:0xf bank_mask:0xf bound_ctrl:1
	ds_write_b32 v32, v24 offset:49200
	ds_bpermute_b32 v24, v36, v128
	s_waitcnt lgkmcnt(0)
	v_mul_lo_u32 v24, v24, s43
	v_add_u32_e32 v28, v24, v35
	v_add_u32_e32 v30, v24, v34
	buffer_load_dwordx4 v[24:27], v28, s[44:47], 0 offen
	buffer_load_dwordx4 v[38:41], v28, s[44:47], s20 offen
	buffer_load_dwordx4 v[44:47], v28, s[44:47], s21 offen
	buffer_load_dwordx4 v[50:53], v28, s[44:47], s23 offen
	s_nop 0
	buffer_load_dwordx2 v[28:29], v30, s[44:47], 0 offen
	buffer_load_dwordx2 v[48:49], v30, s[44:47], s33 offen
	buffer_load_dwordx2 v[42:43], v30, s[44:47], s21 offen
	buffer_load_dwordx2 v[54:55], v30, s[44:47], s94 offen
	s_waitcnt vmcnt(27)
	v_mfma_f32_16x16x128_f8f6f4 v[56:59], v[56:61], v[18:23], 0 cbsz:2 blgp:2
	s_waitcnt vmcnt(26)
	v_mfma_f32_16x16x128_f8f6f4 v[56:59], v[68:73], v[12:17], v[56:59] cbsz:2 blgp:2
	s_waitcnt vmcnt(25)
	v_mfma_f32_16x16x128_f8f6f4 v[56:59], v[62:67], v[6:11], v[56:59] cbsz:2 blgp:2
	s_waitcnt vmcnt(24)
	v_mfma_f32_16x16x128_f8f6f4 v[56:59], v[74:79], v[0:5], v[56:59] cbsz:2 blgp:2
	s_nop 7
	v_cndmask_b32_e64 v30, v56, v57, s[4:5]
	v_cndmask_b32_e64 v30, v30, v58, s[2:3]
	v_cndmask_b32_e32 v30, v30, v59, vcc
	v_mul_f32_e32 v31, v33, v30
	s_nop 1
	v_mov_b32_dpp v31, v31 quad_perm:[1,0,3,2] row_mask:0xf bank_mask:0xf bound_ctrl:1
	v_fmac_f32_e32 v31, v33, v30
	s_nop 1
	v_add_f32_dpp v30, v31, v31 quad_perm:[2,3,0,1] row_mask:0xf bank_mask:0xf bound_ctrl:1
	s_nop 1
	v_add_f32_dpp v30, v30, v30 row_half_mirror row_mask:0xf bank_mask:0xf bound_ctrl:1
	ds_write_b32 v32, v30 offset:49204
	ds_bpermute_b32 v30, v36, v128 offset:16
	s_waitcnt lgkmcnt(0)
	v_mul_lo_u32 v30, v30, s43
	v_add_u32_e32 v31, v30, v35
	v_add_u32_e32 v30, v30, v34
	buffer_load_dwordx4 v[56:59], v31, s[44:47], 0 offen
	buffer_load_dwordx4 v[62:65], v31, s[44:47], s20 offen
	buffer_load_dwordx4 v[68:71], v31, s[44:47], s21 offen
	buffer_load_dwordx4 v[74:77], v31, s[44:47], s23 offen
	buffer_load_dwordx2 v[60:61], v30, s[44:47], 0 offen
	buffer_load_dwordx2 v[72:73], v30, s[44:47], s33 offen
	buffer_load_dwordx2 v[66:67], v30, s[44:47], s21 offen
	buffer_load_dwordx2 v[78:79], v30, s[44:47], s94 offen
	s_waitcnt vmcnt(27)
	v_mfma_f32_16x16x128_f8f6f4 v[86:89], v[86:91], v[18:23], 0 cbsz:2 blgp:2
	s_waitcnt vmcnt(26)
	v_mfma_f32_16x16x128_f8f6f4 v[86:89], v[98:103], v[12:17], v[86:89] cbsz:2 blgp:2
	s_waitcnt vmcnt(25)
	v_mfma_f32_16x16x128_f8f6f4 v[86:89], v[92:97], v[6:11], v[86:89] cbsz:2 blgp:2
	s_waitcnt vmcnt(24)
	v_mfma_f32_16x16x128_f8f6f4 v[86:89], v[150:155], v[0:5], v[86:89] cbsz:2 blgp:2
	s_nop 7
	v_cndmask_b32_e64 v30, v86, v87, s[4:5]
	v_cndmask_b32_e64 v30, v30, v88, s[2:3]
	v_cndmask_b32_e32 v30, v30, v89, vcc
	v_mul_f32_e32 v31, v33, v30
	s_nop 1
	v_mov_b32_dpp v31, v31 quad_perm:[1,0,3,2] row_mask:0xf bank_mask:0xf bound_ctrl:1
	v_fmac_f32_e32 v31, v33, v30
	s_nop 1
	v_add_f32_dpp v30, v31, v31 quad_perm:[2,3,0,1] row_mask:0xf bank_mask:0xf bound_ctrl:1
	s_nop 1
	v_add_f32_dpp v30, v30, v30 row_half_mirror row_mask:0xf bank_mask:0xf bound_ctrl:1
	ds_write_b32 v32, v30 offset:49208
	ds_bpermute_b32 v30, v36, v128 offset:32
	s_waitcnt lgkmcnt(0)
	v_mul_lo_u32 v30, v30, s43
	v_add_u32_e32 v31, v30, v35
	v_add_u32_e32 v30, v30, v34
	buffer_load_dwordx4 v[86:89], v31, s[44:47], 0 offen
	buffer_load_dwordx4 v[92:95], v31, s[44:47], s20 offen
	buffer_load_dwordx4 v[98:101], v31, s[44:47], s21 offen
	buffer_load_dwordx4 v[150:153], v31, s[44:47], s23 offen
	buffer_load_dwordx2 v[90:91], v30, s[44:47], 0 offen
	buffer_load_dwordx2 v[102:103], v30, s[44:47], s33 offen
	buffer_load_dwordx2 v[96:97], v30, s[44:47], s21 offen
	buffer_load_dwordx2 v[154:155], v30, s[44:47], s94 offen
	s_waitcnt vmcnt(27)
	v_mfma_f32_16x16x128_f8f6f4 v[156:159], v[156:161], v[18:23], 0 cbsz:2 blgp:2
	s_waitcnt vmcnt(26)
	v_mfma_f32_16x16x128_f8f6f4 v[156:159], v[168:173], v[12:17], v[156:159] cbsz:2 blgp:2
	s_waitcnt vmcnt(25)
	v_mfma_f32_16x16x128_f8f6f4 v[156:159], v[162:167], v[6:11], v[156:159] cbsz:2 blgp:2
	s_waitcnt vmcnt(24)
	v_mfma_f32_16x16x128_f8f6f4 v[156:159], v[174:179], v[0:5], v[156:159] cbsz:2 blgp:2
	s_nop 7
	v_cndmask_b32_e64 v30, v156, v157, s[4:5]
	v_cndmask_b32_e64 v30, v30, v158, s[2:3]
	v_cndmask_b32_e32 v30, v30, v159, vcc
	v_mul_f32_e32 v31, v33, v30
	s_nop 1
	v_mov_b32_dpp v31, v31 quad_perm:[1,0,3,2] row_mask:0xf bank_mask:0xf bound_ctrl:1
	v_fmac_f32_e32 v31, v33, v30
	s_nop 1
	v_add_f32_dpp v30, v31, v31 quad_perm:[2,3,0,1] row_mask:0xf bank_mask:0xf bound_ctrl:1
	s_nop 1
	v_add_f32_dpp v30, v30, v30 row_half_mirror row_mask:0xf bank_mask:0xf bound_ctrl:1
	ds_write_b32 v32, v30 offset:49212
	ds_bpermute_b32 v30, v36, v128 offset:48
	s_waitcnt lgkmcnt(0)
	v_mul_lo_u32 v30, v30, s43
	v_add_u32_e32 v31, v30, v35
	v_add_u32_e32 v30, v30, v34
	buffer_load_dwordx4 v[156:159], v31, s[44:47], 0 offen
	buffer_load_dwordx4 v[162:165], v31, s[44:47], s20 offen
	buffer_load_dwordx4 v[168:171], v31, s[44:47], s21 offen
	buffer_load_dwordx4 v[174:177], v31, s[44:47], s23 offen
	buffer_load_dwordx2 v[160:161], v30, s[44:47], 0 offen
	buffer_load_dwordx2 v[172:173], v30, s[44:47], s33 offen
	buffer_load_dwordx2 v[166:167], v30, s[44:47], s21 offen
	buffer_load_dwordx2 v[178:179], v30, s[44:47], s94 offen
	s_waitcnt vmcnt(27)
	v_mfma_f32_16x16x128_f8f6f4 v[24:27], v[24:29], v[18:23], 0 cbsz:2 blgp:2
	s_waitcnt vmcnt(26)
	v_mfma_f32_16x16x128_f8f6f4 v[24:27], v[44:49], v[12:17], v[24:27] cbsz:2 blgp:2
	s_waitcnt vmcnt(25)
	v_mfma_f32_16x16x128_f8f6f4 v[24:27], v[38:43], v[6:11], v[24:27] cbsz:2 blgp:2
	s_waitcnt vmcnt(24)
	v_mfma_f32_16x16x128_f8f6f4 v[24:27], v[50:55], v[0:5], v[24:27] cbsz:2 blgp:2
	s_nop 7
	v_cndmask_b32_e64 v24, v24, v25, s[4:5]
	v_cndmask_b32_e64 v24, v24, v26, s[2:3]
	v_cndmask_b32_e32 v24, v24, v27, vcc
	v_mul_f32_e32 v25, v33, v24
	s_nop 1
	v_mov_b32_dpp v25, v25 quad_perm:[1,0,3,2] row_mask:0xf bank_mask:0xf bound_ctrl:1
	v_fmac_f32_e32 v25, v33, v24
	s_nop 1
	v_add_f32_dpp v24, v25, v25 quad_perm:[2,3,0,1] row_mask:0xf bank_mask:0xf bound_ctrl:1
	s_nop 1
	v_add_f32_dpp v24, v24, v24 row_half_mirror row_mask:0xf bank_mask:0xf bound_ctrl:1
	ds_write_b32 v32, v24 offset:49216
	ds_bpermute_b32 v24, v36, v128 offset:64
	s_waitcnt lgkmcnt(0)
	v_mul_lo_u32 v24, v24, s43
	v_add_u32_e32 v28, v24, v35
	v_add_u32_e32 v30, v24, v34
	buffer_load_dwordx4 v[24:27], v28, s[44:47], 0 offen
	buffer_load_dwordx4 v[38:41], v28, s[44:47], s20 offen
	buffer_load_dwordx4 v[44:47], v28, s[44:47], s21 offen
	buffer_load_dwordx4 v[50:53], v28, s[44:47], s23 offen
	s_nop 0
	buffer_load_dwordx2 v[28:29], v30, s[44:47], 0 offen
	buffer_load_dwordx2 v[48:49], v30, s[44:47], s33 offen
	buffer_load_dwordx2 v[42:43], v30, s[44:47], s21 offen
	buffer_load_dwordx2 v[54:55], v30, s[44:47], s94 offen
	s_waitcnt vmcnt(27)
	v_mfma_f32_16x16x128_f8f6f4 v[56:59], v[56:61], v[18:23], 0 cbsz:2 blgp:2
	s_waitcnt vmcnt(26)
	v_mfma_f32_16x16x128_f8f6f4 v[56:59], v[68:73], v[12:17], v[56:59] cbsz:2 blgp:2
	s_waitcnt vmcnt(25)
	v_mfma_f32_16x16x128_f8f6f4 v[56:59], v[62:67], v[6:11], v[56:59] cbsz:2 blgp:2
	s_waitcnt vmcnt(24)
	v_mfma_f32_16x16x128_f8f6f4 v[56:59], v[74:79], v[0:5], v[56:59] cbsz:2 blgp:2
	s_nop 7
	v_cndmask_b32_e64 v30, v56, v57, s[4:5]
	v_cndmask_b32_e64 v30, v30, v58, s[2:3]
	v_cndmask_b32_e32 v30, v30, v59, vcc
	v_mul_f32_e32 v31, v33, v30
	s_nop 1
	v_mov_b32_dpp v31, v31 quad_perm:[1,0,3,2] row_mask:0xf bank_mask:0xf bound_ctrl:1
	v_fmac_f32_e32 v31, v33, v30
	s_nop 1
	v_add_f32_dpp v30, v31, v31 quad_perm:[2,3,0,1] row_mask:0xf bank_mask:0xf bound_ctrl:1
	s_nop 1
	v_add_f32_dpp v30, v30, v30 row_half_mirror row_mask:0xf bank_mask:0xf bound_ctrl:1
	ds_write_b32 v32, v30 offset:49220
	ds_bpermute_b32 v30, v36, v128 offset:80
	s_waitcnt lgkmcnt(0)
	v_mul_lo_u32 v30, v30, s43
	v_add_u32_e32 v31, v30, v35
	v_add_u32_e32 v30, v30, v34
	buffer_load_dwordx4 v[56:59], v31, s[44:47], 0 offen
	buffer_load_dwordx4 v[62:65], v31, s[44:47], s20 offen
	buffer_load_dwordx4 v[68:71], v31, s[44:47], s21 offen
	buffer_load_dwordx4 v[74:77], v31, s[44:47], s23 offen
	buffer_load_dwordx2 v[60:61], v30, s[44:47], 0 offen
	buffer_load_dwordx2 v[72:73], v30, s[44:47], s33 offen
	buffer_load_dwordx2 v[66:67], v30, s[44:47], s21 offen
	buffer_load_dwordx2 v[78:79], v30, s[44:47], s94 offen
	s_waitcnt vmcnt(27)
	v_mfma_f32_16x16x128_f8f6f4 v[86:89], v[86:91], v[18:23], 0 cbsz:2 blgp:2
	s_waitcnt vmcnt(26)
	v_mfma_f32_16x16x128_f8f6f4 v[86:89], v[98:103], v[12:17], v[86:89] cbsz:2 blgp:2
	s_waitcnt vmcnt(25)
	v_mfma_f32_16x16x128_f8f6f4 v[86:89], v[92:97], v[6:11], v[86:89] cbsz:2 blgp:2
	s_waitcnt vmcnt(24)
	v_mfma_f32_16x16x128_f8f6f4 v[86:89], v[150:155], v[0:5], v[86:89] cbsz:2 blgp:2
	s_nop 7
	v_cndmask_b32_e64 v30, v86, v87, s[4:5]
	v_cndmask_b32_e64 v30, v30, v88, s[2:3]
	v_cndmask_b32_e32 v30, v30, v89, vcc
	v_mul_f32_e32 v31, v33, v30
	s_nop 1
	v_mov_b32_dpp v31, v31 quad_perm:[1,0,3,2] row_mask:0xf bank_mask:0xf bound_ctrl:1
	v_fmac_f32_e32 v31, v33, v30
	s_nop 1
	v_add_f32_dpp v30, v31, v31 quad_perm:[2,3,0,1] row_mask:0xf bank_mask:0xf bound_ctrl:1
	s_nop 1
	v_add_f32_dpp v30, v30, v30 row_half_mirror row_mask:0xf bank_mask:0xf bound_ctrl:1
	ds_write_b32 v32, v30 offset:49224
	ds_bpermute_b32 v30, v36, v128 offset:96
	s_waitcnt lgkmcnt(0)
	v_mul_lo_u32 v30, v30, s43
	v_add_u32_e32 v31, v30, v35
	v_add_u32_e32 v30, v30, v34
	buffer_load_dwordx4 v[86:89], v31, s[44:47], 0 offen
	buffer_load_dwordx4 v[92:95], v31, s[44:47], s20 offen
	buffer_load_dwordx4 v[98:101], v31, s[44:47], s21 offen
	buffer_load_dwordx4 v[150:153], v31, s[44:47], s23 offen
	buffer_load_dwordx2 v[90:91], v30, s[44:47], 0 offen
	buffer_load_dwordx2 v[102:103], v30, s[44:47], s33 offen
	buffer_load_dwordx2 v[96:97], v30, s[44:47], s21 offen
	buffer_load_dwordx2 v[154:155], v30, s[44:47], s94 offen
	s_waitcnt vmcnt(27)
	v_mfma_f32_16x16x128_f8f6f4 v[156:159], v[156:161], v[18:23], 0 cbsz:2 blgp:2
	s_waitcnt vmcnt(26)
	v_mfma_f32_16x16x128_f8f6f4 v[156:159], v[168:173], v[12:17], v[156:159] cbsz:2 blgp:2
	s_waitcnt vmcnt(25)
	v_mfma_f32_16x16x128_f8f6f4 v[156:159], v[162:167], v[6:11], v[156:159] cbsz:2 blgp:2
	s_waitcnt vmcnt(24)
	v_mfma_f32_16x16x128_f8f6f4 v[156:159], v[174:179], v[0:5], v[156:159] cbsz:2 blgp:2
	s_nop 7
	v_cndmask_b32_e64 v30, v156, v157, s[4:5]
	v_cndmask_b32_e64 v30, v30, v158, s[2:3]
	v_cndmask_b32_e32 v30, v30, v159, vcc
	v_mul_f32_e32 v31, v33, v30
	s_nop 1
	v_mov_b32_dpp v31, v31 quad_perm:[1,0,3,2] row_mask:0xf bank_mask:0xf bound_ctrl:1
	v_fmac_f32_e32 v31, v33, v30
	s_nop 1
	v_add_f32_dpp v30, v31, v31 quad_perm:[2,3,0,1] row_mask:0xf bank_mask:0xf bound_ctrl:1
	s_nop 1
	v_add_f32_dpp v30, v30, v30 row_half_mirror row_mask:0xf bank_mask:0xf bound_ctrl:1
	ds_write_b32 v32, v30 offset:49228
	ds_bpermute_b32 v30, v36, v128 offset:112
	s_waitcnt lgkmcnt(0)
	v_mul_lo_u32 v30, v30, s43
	v_add_u32_e32 v31, v30, v35
	v_add_u32_e32 v30, v30, v34
	buffer_load_dwordx4 v[156:159], v31, s[44:47], 0 offen
	buffer_load_dwordx4 v[162:165], v31, s[44:47], s20 offen
	buffer_load_dwordx4 v[168:171], v31, s[44:47], s21 offen
	buffer_load_dwordx4 v[174:177], v31, s[44:47], s23 offen
	buffer_load_dwordx2 v[160:161], v30, s[44:47], 0 offen
	buffer_load_dwordx2 v[172:173], v30, s[44:47], s33 offen
	buffer_load_dwordx2 v[166:167], v30, s[44:47], s21 offen
	buffer_load_dwordx2 v[178:179], v30, s[44:47], s94 offen
	s_waitcnt vmcnt(27)
	v_mfma_f32_16x16x128_f8f6f4 v[24:27], v[24:29], v[18:23], 0 cbsz:2 blgp:2
	s_waitcnt vmcnt(26)
	v_mfma_f32_16x16x128_f8f6f4 v[24:27], v[44:49], v[12:17], v[24:27] cbsz:2 blgp:2
	s_waitcnt vmcnt(25)
	v_mfma_f32_16x16x128_f8f6f4 v[24:27], v[38:43], v[6:11], v[24:27] cbsz:2 blgp:2
	s_waitcnt vmcnt(24)
	v_mfma_f32_16x16x128_f8f6f4 v[24:27], v[50:55], v[0:5], v[24:27] cbsz:2 blgp:2
	s_nop 7
	v_cndmask_b32_e64 v24, v24, v25, s[4:5]
	v_cndmask_b32_e64 v24, v24, v26, s[2:3]
	v_cndmask_b32_e32 v24, v24, v27, vcc
	v_mul_f32_e32 v25, v33, v24
	s_nop 1
	v_mov_b32_dpp v25, v25 quad_perm:[1,0,3,2] row_mask:0xf bank_mask:0xf bound_ctrl:1
	v_fmac_f32_e32 v25, v33, v24
	s_nop 1
	v_add_f32_dpp v24, v25, v25 quad_perm:[2,3,0,1] row_mask:0xf bank_mask:0xf bound_ctrl:1
	s_nop 1
	v_add_f32_dpp v24, v24, v24 row_half_mirror row_mask:0xf bank_mask:0xf bound_ctrl:1
	ds_write_b32 v32, v24 offset:49232
	ds_bpermute_b32 v24, v36, v128 offset:128
	s_waitcnt lgkmcnt(0)
	v_mul_lo_u32 v24, v24, s43
	v_add_u32_e32 v28, v24, v35
	v_add_u32_e32 v30, v24, v34
	buffer_load_dwordx4 v[24:27], v28, s[44:47], 0 offen
	buffer_load_dwordx4 v[38:41], v28, s[44:47], s20 offen
	buffer_load_dwordx4 v[44:47], v28, s[44:47], s21 offen
	buffer_load_dwordx4 v[50:53], v28, s[44:47], s23 offen
	s_nop 0
	buffer_load_dwordx2 v[28:29], v30, s[44:47], 0 offen
	buffer_load_dwordx2 v[48:49], v30, s[44:47], s33 offen
	buffer_load_dwordx2 v[42:43], v30, s[44:47], s21 offen
	buffer_load_dwordx2 v[54:55], v30, s[44:47], s94 offen
	s_waitcnt vmcnt(27)
	v_mfma_f32_16x16x128_f8f6f4 v[56:59], v[56:61], v[18:23], 0 cbsz:2 blgp:2
	s_waitcnt vmcnt(26)
	v_mfma_f32_16x16x128_f8f6f4 v[56:59], v[68:73], v[12:17], v[56:59] cbsz:2 blgp:2
	s_waitcnt vmcnt(25)
	v_mfma_f32_16x16x128_f8f6f4 v[56:59], v[62:67], v[6:11], v[56:59] cbsz:2 blgp:2
	s_waitcnt vmcnt(24)
	v_mfma_f32_16x16x128_f8f6f4 v[56:59], v[74:79], v[0:5], v[56:59] cbsz:2 blgp:2
	s_nop 7
	v_cndmask_b32_e64 v30, v56, v57, s[4:5]
	v_cndmask_b32_e64 v30, v30, v58, s[2:3]
	v_cndmask_b32_e32 v30, v30, v59, vcc
	v_mul_f32_e32 v31, v33, v30
	s_nop 1
	v_mov_b32_dpp v31, v31 quad_perm:[1,0,3,2] row_mask:0xf bank_mask:0xf bound_ctrl:1
	v_fmac_f32_e32 v31, v33, v30
	s_nop 1
	v_add_f32_dpp v30, v31, v31 quad_perm:[2,3,0,1] row_mask:0xf bank_mask:0xf bound_ctrl:1
	s_nop 1
	v_add_f32_dpp v30, v30, v30 row_half_mirror row_mask:0xf bank_mask:0xf bound_ctrl:1
	ds_write_b32 v32, v30 offset:49236
	ds_bpermute_b32 v30, v36, v128 offset:144
	s_waitcnt lgkmcnt(0)
	v_mul_lo_u32 v30, v30, s43
	v_add_u32_e32 v31, v30, v35
	v_add_u32_e32 v30, v30, v34
	buffer_load_dwordx4 v[56:59], v31, s[44:47], 0 offen
	buffer_load_dwordx4 v[62:65], v31, s[44:47], s20 offen
	buffer_load_dwordx4 v[68:71], v31, s[44:47], s21 offen
	buffer_load_dwordx4 v[74:77], v31, s[44:47], s23 offen
	buffer_load_dwordx2 v[60:61], v30, s[44:47], 0 offen
	buffer_load_dwordx2 v[72:73], v30, s[44:47], s33 offen
	buffer_load_dwordx2 v[66:67], v30, s[44:47], s21 offen
	buffer_load_dwordx2 v[78:79], v30, s[44:47], s94 offen
	s_waitcnt vmcnt(27)
	v_mfma_f32_16x16x128_f8f6f4 v[86:89], v[86:91], v[18:23], 0 cbsz:2 blgp:2
	s_waitcnt vmcnt(26)
	v_mfma_f32_16x16x128_f8f6f4 v[86:89], v[98:103], v[12:17], v[86:89] cbsz:2 blgp:2
	s_waitcnt vmcnt(25)
	v_mfma_f32_16x16x128_f8f6f4 v[86:89], v[92:97], v[6:11], v[86:89] cbsz:2 blgp:2
	s_waitcnt vmcnt(24)
	v_mfma_f32_16x16x128_f8f6f4 v[86:89], v[150:155], v[0:5], v[86:89] cbsz:2 blgp:2
	s_nop 7
	v_cndmask_b32_e64 v30, v86, v87, s[4:5]
	v_cndmask_b32_e64 v30, v30, v88, s[2:3]
	v_cndmask_b32_e32 v30, v30, v89, vcc
	v_mul_f32_e32 v31, v33, v30
	s_nop 1
	v_mov_b32_dpp v31, v31 quad_perm:[1,0,3,2] row_mask:0xf bank_mask:0xf bound_ctrl:1
	v_fmac_f32_e32 v31, v33, v30
	s_nop 1
	v_add_f32_dpp v30, v31, v31 quad_perm:[2,3,0,1] row_mask:0xf bank_mask:0xf bound_ctrl:1
	s_nop 1
	v_add_f32_dpp v30, v30, v30 row_half_mirror row_mask:0xf bank_mask:0xf bound_ctrl:1
	ds_write_b32 v32, v30 offset:49240
	ds_bpermute_b32 v30, v36, v128 offset:160
	s_waitcnt lgkmcnt(0)
	v_mul_lo_u32 v30, v30, s43
	v_add_u32_e32 v31, v30, v35
	v_add_u32_e32 v30, v30, v34
	buffer_load_dwordx4 v[86:89], v31, s[44:47], 0 offen
	buffer_load_dwordx4 v[92:95], v31, s[44:47], s20 offen
	buffer_load_dwordx4 v[98:101], v31, s[44:47], s21 offen
	buffer_load_dwordx4 v[150:153], v31, s[44:47], s23 offen
	buffer_load_dwordx2 v[90:91], v30, s[44:47], 0 offen
	buffer_load_dwordx2 v[102:103], v30, s[44:47], s33 offen
	buffer_load_dwordx2 v[96:97], v30, s[44:47], s21 offen
	buffer_load_dwordx2 v[154:155], v30, s[44:47], s94 offen
	s_waitcnt vmcnt(27)
	v_mfma_f32_16x16x128_f8f6f4 v[156:159], v[156:161], v[18:23], 0 cbsz:2 blgp:2
	s_waitcnt vmcnt(26)
	v_mfma_f32_16x16x128_f8f6f4 v[156:159], v[168:173], v[12:17], v[156:159] cbsz:2 blgp:2
	s_waitcnt vmcnt(25)
	v_mfma_f32_16x16x128_f8f6f4 v[156:159], v[162:167], v[6:11], v[156:159] cbsz:2 blgp:2
	s_waitcnt vmcnt(24)
	v_mfma_f32_16x16x128_f8f6f4 v[156:159], v[174:179], v[0:5], v[156:159] cbsz:2 blgp:2
	s_nop 7
	v_cndmask_b32_e64 v30, v156, v157, s[4:5]
	v_cndmask_b32_e64 v30, v30, v158, s[2:3]
	v_cndmask_b32_e32 v30, v30, v159, vcc
	v_mul_f32_e32 v31, v33, v30
	s_nop 1
	v_mov_b32_dpp v31, v31 quad_perm:[1,0,3,2] row_mask:0xf bank_mask:0xf bound_ctrl:1
	v_fmac_f32_e32 v31, v33, v30
	s_nop 1
	v_add_f32_dpp v30, v31, v31 quad_perm:[2,3,0,1] row_mask:0xf bank_mask:0xf bound_ctrl:1
	s_nop 1
	v_add_f32_dpp v30, v30, v30 row_half_mirror row_mask:0xf bank_mask:0xf bound_ctrl:1
	ds_write_b32 v32, v30 offset:49244
	ds_bpermute_b32 v30, v36, v128 offset:176
	s_waitcnt lgkmcnt(0)
	v_mul_lo_u32 v30, v30, s43
	v_add_u32_e32 v31, v30, v35
	v_add_u32_e32 v30, v30, v34
	buffer_load_dwordx4 v[156:159], v31, s[44:47], 0 offen
	buffer_load_dwordx4 v[162:165], v31, s[44:47], s20 offen
	buffer_load_dwordx4 v[168:171], v31, s[44:47], s21 offen
	buffer_load_dwordx4 v[174:177], v31, s[44:47], s23 offen
	buffer_load_dwordx2 v[160:161], v30, s[44:47], 0 offen
	buffer_load_dwordx2 v[172:173], v30, s[44:47], s33 offen
	buffer_load_dwordx2 v[166:167], v30, s[44:47], s21 offen
	buffer_load_dwordx2 v[178:179], v30, s[44:47], s94 offen
	s_waitcnt vmcnt(27)
	v_mfma_f32_16x16x128_f8f6f4 v[24:27], v[24:29], v[18:23], 0 cbsz:2 blgp:2
	s_waitcnt vmcnt(26)
	v_mfma_f32_16x16x128_f8f6f4 v[24:27], v[44:49], v[12:17], v[24:27] cbsz:2 blgp:2
	s_waitcnt vmcnt(25)
	v_mfma_f32_16x16x128_f8f6f4 v[24:27], v[38:43], v[6:11], v[24:27] cbsz:2 blgp:2
	s_waitcnt vmcnt(24)
	v_mfma_f32_16x16x128_f8f6f4 v[24:27], v[50:55], v[0:5], v[24:27] cbsz:2 blgp:2
	s_nop 7
	v_cndmask_b32_e64 v24, v24, v25, s[4:5]
	v_cndmask_b32_e64 v24, v24, v26, s[2:3]
	v_cndmask_b32_e32 v24, v24, v27, vcc
	v_mul_f32_e32 v25, v33, v24
	s_nop 1
	v_mov_b32_dpp v25, v25 quad_perm:[1,0,3,2] row_mask:0xf bank_mask:0xf bound_ctrl:1
	v_fmac_f32_e32 v25, v33, v24
	s_nop 1
	v_add_f32_dpp v24, v25, v25 quad_perm:[2,3,0,1] row_mask:0xf bank_mask:0xf bound_ctrl:1
	s_nop 1
	v_add_f32_dpp v24, v24, v24 row_half_mirror row_mask:0xf bank_mask:0xf bound_ctrl:1
	ds_write_b32 v32, v24 offset:49248
	ds_bpermute_b32 v24, v36, v128 offset:192
	s_waitcnt lgkmcnt(0)
	v_mul_lo_u32 v24, v24, s43
	v_add_u32_e32 v28, v24, v35
	v_add_u32_e32 v30, v24, v34
	buffer_load_dwordx4 v[24:27], v28, s[44:47], 0 offen
	buffer_load_dwordx4 v[38:41], v28, s[44:47], s20 offen
	buffer_load_dwordx4 v[44:47], v28, s[44:47], s21 offen
	buffer_load_dwordx4 v[50:53], v28, s[44:47], s23 offen
	s_nop 0
	buffer_load_dwordx2 v[28:29], v30, s[44:47], 0 offen
	buffer_load_dwordx2 v[48:49], v30, s[44:47], s33 offen
	buffer_load_dwordx2 v[42:43], v30, s[44:47], s21 offen
	buffer_load_dwordx2 v[54:55], v30, s[44:47], s94 offen
	s_waitcnt vmcnt(27)
	v_mfma_f32_16x16x128_f8f6f4 v[56:59], v[56:61], v[18:23], 0 cbsz:2 blgp:2
	s_waitcnt vmcnt(26)
	v_mfma_f32_16x16x128_f8f6f4 v[56:59], v[68:73], v[12:17], v[56:59] cbsz:2 blgp:2
	s_waitcnt vmcnt(25)
	v_mfma_f32_16x16x128_f8f6f4 v[56:59], v[62:67], v[6:11], v[56:59] cbsz:2 blgp:2
	s_waitcnt vmcnt(24)
	v_mfma_f32_16x16x128_f8f6f4 v[56:59], v[74:79], v[0:5], v[56:59] cbsz:2 blgp:2
	s_nop 7
	v_cndmask_b32_e64 v30, v56, v57, s[4:5]
	v_cndmask_b32_e64 v30, v30, v58, s[2:3]
	v_cndmask_b32_e32 v30, v30, v59, vcc
	v_mul_f32_e32 v31, v33, v30
	s_nop 1
	v_mov_b32_dpp v31, v31 quad_perm:[1,0,3,2] row_mask:0xf bank_mask:0xf bound_ctrl:1
	v_fmac_f32_e32 v31, v33, v30
	s_nop 1
	v_add_f32_dpp v30, v31, v31 quad_perm:[2,3,0,1] row_mask:0xf bank_mask:0xf bound_ctrl:1
	s_nop 1
	v_add_f32_dpp v30, v30, v30 row_half_mirror row_mask:0xf bank_mask:0xf bound_ctrl:1
	ds_write_b32 v32, v30 offset:49252
	ds_bpermute_b32 v30, v36, v128 offset:208
	s_waitcnt lgkmcnt(0)
	v_mul_lo_u32 v30, v30, s43
	v_add_u32_e32 v31, v30, v35
	v_add_u32_e32 v30, v30, v34
	buffer_load_dwordx4 v[56:59], v31, s[44:47], 0 offen
	buffer_load_dwordx4 v[62:65], v31, s[44:47], s20 offen
	buffer_load_dwordx4 v[68:71], v31, s[44:47], s21 offen
	buffer_load_dwordx4 v[74:77], v31, s[44:47], s23 offen
	buffer_load_dwordx2 v[60:61], v30, s[44:47], 0 offen
	buffer_load_dwordx2 v[72:73], v30, s[44:47], s33 offen
	buffer_load_dwordx2 v[66:67], v30, s[44:47], s21 offen
	buffer_load_dwordx2 v[78:79], v30, s[44:47], s94 offen
	s_waitcnt vmcnt(27)
	v_mfma_f32_16x16x128_f8f6f4 v[86:89], v[86:91], v[18:23], 0 cbsz:2 blgp:2
	s_waitcnt vmcnt(26)
	v_mfma_f32_16x16x128_f8f6f4 v[86:89], v[98:103], v[12:17], v[86:89] cbsz:2 blgp:2
	s_waitcnt vmcnt(25)
	v_mfma_f32_16x16x128_f8f6f4 v[86:89], v[92:97], v[6:11], v[86:89] cbsz:2 blgp:2
	s_waitcnt vmcnt(24)
	v_mfma_f32_16x16x128_f8f6f4 v[86:89], v[150:155], v[0:5], v[86:89] cbsz:2 blgp:2
	s_nop 7
	v_cndmask_b32_e64 v30, v86, v87, s[4:5]
	v_cndmask_b32_e64 v30, v30, v88, s[2:3]
	v_cndmask_b32_e32 v30, v30, v89, vcc
	v_mul_f32_e32 v31, v33, v30
	s_nop 1
	v_mov_b32_dpp v31, v31 quad_perm:[1,0,3,2] row_mask:0xf bank_mask:0xf bound_ctrl:1
	v_fmac_f32_e32 v31, v33, v30
	s_nop 1
	v_add_f32_dpp v30, v31, v31 quad_perm:[2,3,0,1] row_mask:0xf bank_mask:0xf bound_ctrl:1
	s_nop 1
	v_add_f32_dpp v30, v30, v30 row_half_mirror row_mask:0xf bank_mask:0xf bound_ctrl:1
	ds_write_b32 v32, v30 offset:49256
	ds_bpermute_b32 v30, v36, v128 offset:224
	s_waitcnt lgkmcnt(0)
	v_mul_lo_u32 v30, v30, s43
	v_add_u32_e32 v31, v30, v35
	v_add_u32_e32 v30, v30, v34
	buffer_load_dwordx4 v[86:89], v31, s[44:47], 0 offen
	buffer_load_dwordx4 v[92:95], v31, s[44:47], s20 offen
	buffer_load_dwordx4 v[98:101], v31, s[44:47], s21 offen
	buffer_load_dwordx4 v[150:153], v31, s[44:47], s23 offen
	buffer_load_dwordx2 v[90:91], v30, s[44:47], 0 offen
	buffer_load_dwordx2 v[102:103], v30, s[44:47], s33 offen
	buffer_load_dwordx2 v[96:97], v30, s[44:47], s21 offen
	buffer_load_dwordx2 v[154:155], v30, s[44:47], s94 offen
	s_waitcnt vmcnt(27)
	v_mfma_f32_16x16x128_f8f6f4 v[156:159], v[156:161], v[18:23], 0 cbsz:2 blgp:2
	s_waitcnt vmcnt(26)
	v_mfma_f32_16x16x128_f8f6f4 v[156:159], v[168:173], v[12:17], v[156:159] cbsz:2 blgp:2
	s_waitcnt vmcnt(25)
	v_mfma_f32_16x16x128_f8f6f4 v[156:159], v[162:167], v[6:11], v[156:159] cbsz:2 blgp:2
	s_waitcnt vmcnt(24)
	v_mfma_f32_16x16x128_f8f6f4 v[156:159], v[174:179], v[0:5], v[156:159] cbsz:2 blgp:2
	s_nop 7
	v_cndmask_b32_e64 v30, v156, v157, s[4:5]
	v_cndmask_b32_e64 v30, v30, v158, s[2:3]
	v_cndmask_b32_e32 v30, v30, v159, vcc
	v_mul_f32_e32 v31, v33, v30
	s_nop 1
	v_mov_b32_dpp v31, v31 quad_perm:[1,0,3,2] row_mask:0xf bank_mask:0xf bound_ctrl:1
	v_fmac_f32_e32 v31, v33, v30
	s_nop 1
	v_add_f32_dpp v30, v31, v31 quad_perm:[2,3,0,1] row_mask:0xf bank_mask:0xf bound_ctrl:1
	s_nop 1
	v_add_f32_dpp v30, v30, v30 row_half_mirror row_mask:0xf bank_mask:0xf bound_ctrl:1
	ds_write_b32 v32, v30 offset:49260
	ds_bpermute_b32 v30, v36, v128 offset:240
	s_waitcnt lgkmcnt(0)
	v_mul_lo_u32 v30, v30, s43
	v_add_u32_e32 v31, v30, v35
	v_add_u32_e32 v30, v30, v34
	buffer_load_dwordx4 v[156:159], v31, s[44:47], 0 offen
	buffer_load_dwordx4 v[162:165], v31, s[44:47], s20 offen
	buffer_load_dwordx4 v[168:171], v31, s[44:47], s21 offen
	buffer_load_dwordx4 v[174:177], v31, s[44:47], s23 offen
	buffer_load_dwordx2 v[160:161], v30, s[44:47], 0 offen
	buffer_load_dwordx2 v[172:173], v30, s[44:47], s33 offen
	buffer_load_dwordx2 v[166:167], v30, s[44:47], s21 offen
	buffer_load_dwordx2 v[178:179], v30, s[44:47], s94 offen
	s_waitcnt vmcnt(27)
	v_mfma_f32_16x16x128_f8f6f4 v[24:27], v[24:29], v[18:23], 0 cbsz:2 blgp:2
	s_waitcnt vmcnt(26)
	v_mfma_f32_16x16x128_f8f6f4 v[24:27], v[44:49], v[12:17], v[24:27] cbsz:2 blgp:2
	s_waitcnt vmcnt(25)
	v_mfma_f32_16x16x128_f8f6f4 v[24:27], v[38:43], v[6:11], v[24:27] cbsz:2 blgp:2
	s_waitcnt vmcnt(24)
	v_mfma_f32_16x16x128_f8f6f4 v[24:27], v[50:55], v[0:5], v[24:27] cbsz:2 blgp:2
	s_nop 7
	v_cndmask_b32_e64 v24, v24, v25, s[4:5]
	v_cndmask_b32_e64 v24, v24, v26, s[2:3]
	v_cndmask_b32_e32 v24, v24, v27, vcc
	v_mul_f32_e32 v25, v33, v24
	s_nop 1
	v_mov_b32_dpp v25, v25 quad_perm:[1,0,3,2] row_mask:0xf bank_mask:0xf bound_ctrl:1
	v_fmac_f32_e32 v25, v33, v24
	s_nop 1
	v_add_f32_dpp v24, v25, v25 quad_perm:[2,3,0,1] row_mask:0xf bank_mask:0xf bound_ctrl:1
	s_nop 1
	v_add_f32_dpp v24, v24, v24 row_half_mirror row_mask:0xf bank_mask:0xf bound_ctrl:1
	ds_write_b32 v32, v24 offset:49264
	s_waitcnt vmcnt(19)
	v_mfma_f32_16x16x128_f8f6f4 v[24:27], v[56:61], v[18:23], 0 cbsz:2 blgp:2
	s_waitcnt vmcnt(18)
	v_mfma_f32_16x16x128_f8f6f4 v[24:27], v[68:73], v[12:17], v[24:27] cbsz:2 blgp:2
	s_waitcnt vmcnt(17)
	v_mfma_f32_16x16x128_f8f6f4 v[24:27], v[62:67], v[6:11], v[24:27] cbsz:2 blgp:2
	s_waitcnt vmcnt(16)
	v_mfma_f32_16x16x128_f8f6f4 v[24:27], v[74:79], v[0:5], v[24:27] cbsz:2 blgp:2
	s_nop 7
	v_cndmask_b32_e64 v24, v24, v25, s[4:5]
	v_cndmask_b32_e64 v24, v24, v26, s[2:3]
	v_cndmask_b32_e32 v24, v24, v27, vcc
	v_mul_f32_e32 v25, v33, v24
	s_nop 1
	v_mov_b32_dpp v25, v25 quad_perm:[1,0,3,2] row_mask:0xf bank_mask:0xf bound_ctrl:1
	v_fmac_f32_e32 v25, v33, v24
	s_nop 1
	v_add_f32_dpp v24, v25, v25 quad_perm:[2,3,0,1] row_mask:0xf bank_mask:0xf bound_ctrl:1
	s_nop 1
	v_add_f32_dpp v24, v24, v24 row_half_mirror row_mask:0xf bank_mask:0xf bound_ctrl:1
	ds_write_b32 v32, v24 offset:49268
	s_waitcnt vmcnt(11)
	v_mfma_f32_16x16x128_f8f6f4 v[24:27], v[86:91], v[18:23], 0 cbsz:2 blgp:2
	s_waitcnt vmcnt(10)
	v_mfma_f32_16x16x128_f8f6f4 v[24:27], v[98:103], v[12:17], v[24:27] cbsz:2 blgp:2
	s_waitcnt vmcnt(9)
	v_mfma_f32_16x16x128_f8f6f4 v[24:27], v[92:97], v[6:11], v[24:27] cbsz:2 blgp:2
	s_waitcnt vmcnt(8)
	v_mfma_f32_16x16x128_f8f6f4 v[24:27], v[150:155], v[0:5], v[24:27] cbsz:2 blgp:2
	s_nop 7
	v_cndmask_b32_e64 v24, v24, v25, s[4:5]
	v_cndmask_b32_e64 v24, v24, v26, s[2:3]
	v_cndmask_b32_e32 v24, v24, v27, vcc
	v_mul_f32_e32 v25, v33, v24
	s_nop 1
	v_mov_b32_dpp v25, v25 quad_perm:[1,0,3,2] row_mask:0xf bank_mask:0xf bound_ctrl:1
	v_fmac_f32_e32 v25, v33, v24
	s_nop 1
	v_add_f32_dpp v24, v25, v25 quad_perm:[2,3,0,1] row_mask:0xf bank_mask:0xf bound_ctrl:1
	s_nop 1
	v_add_f32_dpp v24, v24, v24 row_half_mirror row_mask:0xf bank_mask:0xf bound_ctrl:1
	ds_write_b32 v32, v24 offset:49272
	s_waitcnt vmcnt(3)
	v_mfma_f32_16x16x128_f8f6f4 v[18:21], v[156:161], v[18:23], 0 cbsz:2 blgp:2
	s_waitcnt vmcnt(2)
	v_mfma_f32_16x16x128_f8f6f4 v[12:15], v[168:173], v[12:17], v[18:21] cbsz:2 blgp:2
	s_waitcnt vmcnt(1)
	v_mfma_f32_16x16x128_f8f6f4 v[6:9], v[162:167], v[6:11], v[12:15] cbsz:2 blgp:2
	s_waitcnt vmcnt(0)
	v_mfma_f32_16x16x128_f8f6f4 v[0:3], v[174:179], v[0:5], v[6:9] cbsz:2 blgp:2
	s_nop 7
	v_cndmask_b32_e64 v0, v0, v1, s[4:5]
	v_cndmask_b32_e64 v0, v0, v2, s[2:3]
	v_cndmask_b32_e32 v0, v0, v3, vcc
	v_mul_f32_e32 v1, v33, v0
	s_nop 1
	v_mov_b32_dpp v1, v1 quad_perm:[1,0,3,2] row_mask:0xf bank_mask:0xf bound_ctrl:1
	v_fmac_f32_e32 v1, v33, v0
	s_nop 1
	v_add_f32_dpp v0, v1, v1 quad_perm:[2,3,0,1] row_mask:0xf bank_mask:0xf bound_ctrl:1
	s_nop 1
	v_add_f32_dpp v0, v0, v0 row_half_mirror row_mask:0xf bank_mask:0xf bound_ctrl:1
	ds_write_b32 v32, v0 offset:49276
	v_mul_u32_u24_e32 v240, 0x600, v130
	v_mul_u32_u24_e32 v241, 0x600, v128
	v_add_u32_e32 v240, 0x8000000, v240
	v_add_u32_e32 v241, 0x8000000, v241
	v_lshrrev_b32_e32 v0, 1, v129
	v_readlane_b32 s100, v240, 0
	v_readlane_b32 s101, v240, 1
	v_readlane_b32 s2, v240, 2
	v_readlane_b32 s3, v240, 3
	s_nop 1
	buffer_load_dwordx4 v[74:77], v129, s[44:47], s100 offen
	buffer_load_dwordx2 v[78:79], v0, s[44:47], s100 offen offset:1024
	buffer_load_dwordx4 v[68:71], v129, s[44:47], s101 offen
	buffer_load_dwordx2 v[72:73], v0, s[44:47], s101 offen offset:1024
	buffer_load_dwordx4 v[56:59], v129, s[44:47], s2 offen
	buffer_load_dwordx2 v[60:61], v0, s[44:47], s2 offen offset:1024
	buffer_load_dwordx4 v[44:47], v129, s[44:47], s3 offen
	buffer_load_dwordx2 v[48:49], v0, s[44:47], s3 offen offset:1024
	v_add_u32_e32 v210, 0x400, v0
	v_readlane_b32 s100, v240, 4
	v_readlane_b32 s101, v240, 5
	v_readlane_b32 s2, v240, 6
	v_readlane_b32 s3, v240, 7
	s_nop 1
	buffer_load_dwordx4 v[62:65], v129, s[44:47], s100 offen
	buffer_load_dwordx2 v[66:67], v0, s[44:47], s100 offen offset:1024
	buffer_load_dwordx4 v[50:53], v129, s[44:47], s101 offen
	buffer_load_dwordx2 v[54:55], v0, s[44:47], s101 offen offset:1024
	buffer_load_dwordx4 v[38:41], v129, s[44:47], s2 offen
	buffer_load_dwordx2 v[42:43], v0, s[44:47], s2 offen offset:1024
	buffer_load_dwordx4 v[32:35], v129, s[44:47], s3 offen
	buffer_load_dwordx2 v[36:37], v0, s[44:47], s3 offen offset:1024
	v_div_scale_f32 v2, s[2:3], v80, v80, 1.0
	v_rcp_f32_e32 v3, v2
	v_div_scale_f32 v4, vcc, 1.0, v80, 1.0
	v_and_b32_e32 v1, -4, v148
	v_fma_f32 v0, -v2, v3, 1.0
	v_fmac_f32_e32 v3, v0, v3
	v_mul_f32_e32 v5, v4, v3
	v_fma_f32 v0, -v2, v5, v4
	v_fmac_f32_e32 v5, v0, v3
	v_lshlrev_b32_e32 v0, 7, v148
	v_and_b32_e32 v0, 0x180, v0
	v_add3_u32 v0, v111, v0, v1
	v_add_u32_e32 v0, 0xc000, v0
	ds_read2_b32 v[0:1], v0 offset1:16
	v_fma_f32 v2, -v2, v5, v4
	v_div_fmas_f32 v2, v2, v3, v5
	v_div_fixup_f32 v2, v2, v80, 1.0
	s_mov_b32 s1, 0x3e6d3388
	s_waitcnt lgkmcnt(0)
	v_mul_f32_e32 v0, v2, v0
	v_mul_f32_e32 v0, v83, v0
	v_fma_f32 v3, |v0|, s1, 1.0
	v_rcp_f32_e32 v3, v3
	v_mul_f32_e32 v5, v0, v0
	v_mul_f32_e32 v5, 0xbf38aa3b, v5
	v_exp_f32_e32 v5, v5
	v_fmamk_f32 v4, v3, 0x3f07dc22, v184
	v_fmaak_f32 v4, v3, v4, 0x3f35f0e3
	v_fmaak_f32 v4, v3, v4, 0xbe11a98e
	v_mul_f32_e32 v1, v2, v1
	v_fmaak_f32 v4, v3, v4, 0x3e027906
	v_mul_f32_e32 v3, v3, v4
	v_mul_f32_e32 v1, v82, v1
	v_mul_f32_e32 v3, v5, v3
	v_fma_f32 v5, |v1|, s1, 1.0
	v_rcp_f32_e32 v5, v5
	v_mul_f32_e32 v4, v0, v3
	v_fma_f32 v3, -v0, v3, v0
	v_cmp_gt_f32_e32 vcc, 0, v0
	v_mul_f32_e32 v2, v206, v84
	v_mov_b32_e32 v180, 0
	v_cndmask_b32_e32 v0, v3, v4, vcc
	v_mul_f32_e32 v211, v2, v0
	v_mul_f32_e32 v2, v1, v1
	v_fmamk_f32 v0, v5, 0x3f07dc22, v184
	v_mul_f32_e32 v2, 0xbf38aa3b, v2
	v_fmaak_f32 v0, v5, v0, 0x3f35f0e3
	v_exp_f32_e32 v2, v2
	v_fmaak_f32 v0, v5, v0, 0xbe11a98e
	v_fmaak_f32 v0, v5, v0, 0x3e027906
	v_mul_f32_e32 v0, v5, v0
	v_mul_f32_e32 v0, v2, v0
	v_mul_f32_e32 v2, v1, v0
	v_fma_f32 v0, -v1, v0, v1
	v_cmp_gt_f32_e32 vcc, 0, v1
	v_mul_f32_e32 v1, v205, v81
	v_mov_b32_e32 v181, v180
	v_cndmask_b32_e32 v0, v0, v2, vcc
	v_mul_f32_e32 v131, v1, v0
	v_mov_b32_e32 v178, v180
	v_mov_b32_e32 v179, v180
	v_mov_b32_e32 v176, v180
	v_mov_b32_e32 v177, v180
	v_mov_b32_e32 v174, v180
	v_mov_b32_e32 v175, v180
	v_mov_b32_e32 v172, v180
	v_mov_b32_e32 v173, v180
	v_mov_b32_e32 v170, v180
	v_mov_b32_e32 v171, v180
	v_mov_b32_e32 v168, v180
	v_mov_b32_e32 v169, v180
	v_mov_b32_e32 v166, v180
	v_mov_b32_e32 v167, v180
	v_mov_b32_e32 v164, v180
	v_mov_b32_e32 v165, v180
	v_mov_b32_e32 v162, v180
	v_mov_b32_e32 v163, v180
	v_mov_b32_e32 v160, v180
	v_mov_b32_e32 v161, v180
	v_mov_b32_e32 v158, v180
	v_mov_b32_e32 v159, v180
	v_mov_b32_e32 v156, v180
	v_mov_b32_e32 v157, v180
	v_mov_b32_e32 v154, v180
	v_mov_b32_e32 v155, v180
	v_mov_b32_e32 v152, v180
	v_mov_b32_e32 v153, v180
	v_mov_b32_e32 v150, v180
	v_mov_b32_e32 v151, v180
.LBB0_1139:
	s_cmp_lt_u32 s0, 56
	s_cselect_b64 vcc, -1, 0
	s_add_i32 s6, s0, 8
	s_add_i32 s5, s0, 9
	v_cndmask_b32_e32 v0, v241, v240, vcc
	s_add_i32 s4, s0, 10
	s_add_i32 s1, s0, 11
	v_readlane_b32 s2, v0, s6
	v_readlane_b32 s3, v0, s5
	v_readlane_b32 s100, v0, s4
	v_readlane_b32 s101, v0, s1
	s_nop 1
	buffer_load_dwordx4 v[98:101], v129, s[44:47], s2 offen
	buffer_load_dwordx2 v[102:103], v210, s[44:47], s2 offen
	buffer_load_dwordx4 v[92:95], v129, s[44:47], s3 offen
	buffer_load_dwordx2 v[96:97], v210, s[44:47], s3 offen
	buffer_load_dwordx4 v[86:89], v129, s[44:47], s100 offen
	buffer_load_dwordx2 v[90:91], v210, s[44:47], s100 offen
	buffer_load_dwordx4 v[80:83], v129, s[44:47], s101 offen
	buffer_load_dwordx2 v[84:85], v210, s[44:47], s101 offen
	s_cmp_lt_u32 s0, 64
	s_cselect_b64 s[2:3], -1, 0
	v_cndmask_b32_e64 v188, v131, v211, s[2:3]
	s_waitcnt vmcnt(22)
	v_cvt_scalef32_pk32_f32_fp6 v[0:31], v[74:79], 1.0
	v_readlane_b32 s2, v188, s0
	s_nop 1
	v_pk_fma_f32 v[74:75], v[0:1], s[2:3], v[180:181] op_sel_hi:[1,0,1]
	v_pk_fma_f32 v[76:77], v[2:3], s[2:3], v[178:179] op_sel_hi:[1,0,1]
	v_pk_fma_f32 v[78:79], v[4:5], s[2:3], v[176:177] op_sel_hi:[1,0,1]
	v_pk_fma_f32 v[174:175], v[6:7], s[2:3], v[174:175] op_sel_hi:[1,0,1]
	v_pk_fma_f32 v[172:173], v[8:9], s[2:3], v[172:173] op_sel_hi:[1,0,1]
	v_pk_fma_f32 v[170:171], v[10:11], s[2:3], v[170:171] op_sel_hi:[1,0,1]
	v_pk_fma_f32 v[168:169], v[12:13], s[2:3], v[168:169] op_sel_hi:[1,0,1]
	v_pk_fma_f32 v[166:167], v[14:15], s[2:3], v[166:167] op_sel_hi:[1,0,1]
	v_pk_fma_f32 v[164:165], v[16:17], s[2:3], v[164:165] op_sel_hi:[1,0,1]
	v_pk_fma_f32 v[162:163], v[18:19], s[2:3], v[162:163] op_sel_hi:[1,0,1]
	v_pk_fma_f32 v[160:161], v[20:21], s[2:3], v[160:161] op_sel_hi:[1,0,1]
	v_pk_fma_f32 v[158:159], v[22:23], s[2:3], v[158:159] op_sel_hi:[1,0,1]
	v_pk_fma_f32 v[156:157], v[24:25], s[2:3], v[156:157] op_sel_hi:[1,0,1]
	v_pk_fma_f32 v[154:155], v[26:27], s[2:3], v[154:155] op_sel_hi:[1,0,1]
	v_pk_fma_f32 v[152:153], v[28:29], s[2:3], v[152:153] op_sel_hi:[1,0,1]
	v_pk_fma_f32 v[150:151], v[30:31], s[2:3], v[150:151] op_sel_hi:[1,0,1]
	s_add_i32 s2, s0, 1
	v_readlane_b32 s2, v188, s2
	s_waitcnt vmcnt(20)
	v_cvt_scalef32_pk32_f32_fp6 v[0:31], v[68:73], 1.0
	v_pk_fma_f32 v[68:69], v[0:1], s[2:3], v[74:75] op_sel_hi:[1,0,1]
	v_pk_fma_f32 v[70:71], v[2:3], s[2:3], v[76:77] op_sel_hi:[1,0,1]
	v_pk_fma_f32 v[72:73], v[4:5], s[2:3], v[78:79] op_sel_hi:[1,0,1]
	v_pk_fma_f32 v[74:75], v[6:7], s[2:3], v[174:175] op_sel_hi:[1,0,1]
	v_pk_fma_f32 v[76:77], v[8:9], s[2:3], v[172:173] op_sel_hi:[1,0,1]
	v_pk_fma_f32 v[78:79], v[10:11], s[2:3], v[170:171] op_sel_hi:[1,0,1]
	v_pk_fma_f32 v[168:169], v[12:13], s[2:3], v[168:169] op_sel_hi:[1,0,1]
	v_pk_fma_f32 v[166:167], v[14:15], s[2:3], v[166:167] op_sel_hi:[1,0,1]
	v_pk_fma_f32 v[164:165], v[16:17], s[2:3], v[164:165] op_sel_hi:[1,0,1]
	v_pk_fma_f32 v[162:163], v[18:19], s[2:3], v[162:163] op_sel_hi:[1,0,1]
	v_pk_fma_f32 v[160:161], v[20:21], s[2:3], v[160:161] op_sel_hi:[1,0,1]
	v_pk_fma_f32 v[158:159], v[22:23], s[2:3], v[158:159] op_sel_hi:[1,0,1]
	v_pk_fma_f32 v[156:157], v[24:25], s[2:3], v[156:157] op_sel_hi:[1,0,1]
	v_pk_fma_f32 v[154:155], v[26:27], s[2:3], v[154:155] op_sel_hi:[1,0,1]
	v_pk_fma_f32 v[152:153], v[28:29], s[2:3], v[152:153] op_sel_hi:[1,0,1]
	v_pk_fma_f32 v[150:151], v[30:31], s[2:3], v[150:151] op_sel_hi:[1,0,1]
	s_add_i32 s2, s0, 2
	v_readlane_b32 s2, v188, s2
	s_waitcnt vmcnt(18)
	v_cvt_scalef32_pk32_f32_fp6 v[0:31], v[56:61], 1.0
	v_pk_fma_f32 v[56:57], v[0:1], s[2:3], v[68:69] op_sel_hi:[1,0,1]
	v_pk_fma_f32 v[58:59], v[2:3], s[2:3], v[70:71] op_sel_hi:[1,0,1]
	v_pk_fma_f32 v[60:61], v[4:5], s[2:3], v[72:73] op_sel_hi:[1,0,1]
	v_pk_fma_f32 v[68:69], v[6:7], s[2:3], v[74:75] op_sel_hi:[1,0,1]
	v_pk_fma_f32 v[70:71], v[8:9], s[2:3], v[76:77] op_sel_hi:[1,0,1]
	v_pk_fma_f32 v[72:73], v[10:11], s[2:3], v[78:79] op_sel_hi:[1,0,1]
	v_pk_fma_f32 v[74:75], v[12:13], s[2:3], v[168:169] op_sel_hi:[1,0,1]
	v_pk_fma_f32 v[76:77], v[14:15], s[2:3], v[166:167] op_sel_hi:[1,0,1]
	v_pk_fma_f32 v[78:79], v[16:17], s[2:3], v[164:165] op_sel_hi:[1,0,1]
	v_pk_fma_f32 v[162:163], v[18:19], s[2:3], v[162:163] op_sel_hi:[1,0,1]
	v_pk_fma_f32 v[160:161], v[20:21], s[2:3], v[160:161] op_sel_hi:[1,0,1]
	v_pk_fma_f32 v[158:159], v[22:23], s[2:3], v[158:159] op_sel_hi:[1,0,1]
	v_pk_fma_f32 v[156:157], v[24:25], s[2:3], v[156:157] op_sel_hi:[1,0,1]
	v_pk_fma_f32 v[154:155], v[26:27], s[2:3], v[154:155] op_sel_hi:[1,0,1]
	v_pk_fma_f32 v[152:153], v[28:29], s[2:3], v[152:153] op_sel_hi:[1,0,1]
	v_pk_fma_f32 v[150:151], v[30:31], s[2:3], v[150:151] op_sel_hi:[1,0,1]
	s_add_i32 s2, s0, 3
	v_readlane_b32 s2, v188, s2
	s_waitcnt vmcnt(16)
	v_cvt_scalef32_pk32_f32_fp6 v[0:31], v[44:49], 1.0
	v_pk_fma_f32 v[164:165], v[0:1], s[2:3], v[56:57] op_sel_hi:[1,0,1]
	v_pk_fma_f32 v[166:167], v[2:3], s[2:3], v[58:59] op_sel_hi:[1,0,1]
	v_pk_fma_f32 v[168:169], v[4:5], s[2:3], v[60:61] op_sel_hi:[1,0,1]
	v_pk_fma_f32 v[170:171], v[6:7], s[2:3], v[68:69] op_sel_hi:[1,0,1]
	v_pk_fma_f32 v[172:173], v[8:9], s[2:3], v[70:71] op_sel_hi:[1,0,1]
	v_pk_fma_f32 v[174:175], v[10:11], s[2:3], v[72:73] op_sel_hi:[1,0,1]
	v_pk_fma_f32 v[176:177], v[12:13], s[2:3], v[74:75] op_sel_hi:[1,0,1]
	v_pk_fma_f32 v[178:179], v[14:15], s[2:3], v[76:77] op_sel_hi:[1,0,1]
	v_pk_fma_f32 v[180:181], v[16:17], s[2:3], v[78:79] op_sel_hi:[1,0,1]
	v_pk_fma_f32 v[162:163], v[18:19], s[2:3], v[162:163] op_sel_hi:[1,0,1]
	v_pk_fma_f32 v[160:161], v[20:21], s[2:3], v[160:161] op_sel_hi:[1,0,1]
	v_pk_fma_f32 v[158:159], v[22:23], s[2:3], v[158:159] op_sel_hi:[1,0,1]
	v_pk_fma_f32 v[156:157], v[24:25], s[2:3], v[156:157] op_sel_hi:[1,0,1]
	v_pk_fma_f32 v[154:155], v[26:27], s[2:3], v[154:155] op_sel_hi:[1,0,1]
	v_pk_fma_f32 v[152:153], v[28:29], s[2:3], v[152:153] op_sel_hi:[1,0,1]
	v_pk_fma_f32 v[150:151], v[30:31], s[2:3], v[150:151] op_sel_hi:[1,0,1]
	s_cmp_lt_u32 s0, 52
	s_cselect_b64 s[2:3], -1, 0
	s_add_i32 s7, s0, 12
	s_add_i32 s100, s0, 13
	v_cndmask_b32_e64 v0, v241, v240, s[2:3]
	s_add_i32 s101, s0, 14
	s_nop 0
	v_readlane_b32 s2, v0, s7
	s_add_i32 s3, s0, 15
	v_readlane_b32 s100, v0, s100
	v_readlane_b32 s101, v0, s101
	v_readlane_b32 s3, v0, s3
	s_nop 1
	buffer_load_dwordx4 v[74:77], v129, s[44:47], s2 offen
	buffer_load_dwordx2 v[78:79], v210, s[44:47], s2 offen
	buffer_load_dwordx4 v[68:71], v129, s[44:47], s100 offen
	buffer_load_dwordx2 v[72:73], v210, s[44:47], s100 offen
	buffer_load_dwordx4 v[56:59], v129, s[44:47], s101 offen
	buffer_load_dwordx2 v[60:61], v210, s[44:47], s101 offen
	buffer_load_dwordx4 v[44:47], v129, s[44:47], s3 offen
	buffer_load_dwordx2 v[48:49], v210, s[44:47], s3 offen
	s_cmp_lt_u32 s0, 60
	s_cselect_b64 s[2:3], -1, 0
	v_cndmask_b32_e64 v188, v131, v211, s[2:3]
	s_add_i32 s2, s0, 4
	v_readlane_b32 s2, v188, s2
	s_waitcnt vmcnt(22)
	v_cvt_scalef32_pk32_f32_fp6 v[0:31], v[62:67], 1.0
	v_pk_fma_f32 v[62:63], v[0:1], s[2:3], v[164:165] op_sel_hi:[1,0,1]
	v_pk_fma_f32 v[64:65], v[2:3], s[2:3], v[166:167] op_sel_hi:[1,0,1]
	v_pk_fma_f32 v[66:67], v[4:5], s[2:3], v[168:169] op_sel_hi:[1,0,1]
	v_pk_fma_f32 v[164:165], v[6:7], s[2:3], v[170:171] op_sel_hi:[1,0,1]
	v_pk_fma_f32 v[166:167], v[8:9], s[2:3], v[172:173] op_sel_hi:[1,0,1]
	v_pk_fma_f32 v[168:169], v[10:11], s[2:3], v[174:175] op_sel_hi:[1,0,1]
	v_pk_fma_f32 v[170:171], v[12:13], s[2:3], v[176:177] op_sel_hi:[1,0,1]
	v_pk_fma_f32 v[172:173], v[14:15], s[2:3], v[178:179] op_sel_hi:[1,0,1]
	v_pk_fma_f32 v[174:175], v[16:17], s[2:3], v[180:181] op_sel_hi:[1,0,1]
	v_pk_fma_f32 v[162:163], v[18:19], s[2:3], v[162:163] op_sel_hi:[1,0,1]
	v_pk_fma_f32 v[160:161], v[20:21], s[2:3], v[160:161] op_sel_hi:[1,0,1]
	v_pk_fma_f32 v[158:159], v[22:23], s[2:3], v[158:159] op_sel_hi:[1,0,1]
	v_pk_fma_f32 v[156:157], v[24:25], s[2:3], v[156:157] op_sel_hi:[1,0,1]
	v_pk_fma_f32 v[154:155], v[26:27], s[2:3], v[154:155] op_sel_hi:[1,0,1]
	v_pk_fma_f32 v[152:153], v[28:29], s[2:3], v[152:153] op_sel_hi:[1,0,1]
	v_pk_fma_f32 v[150:151], v[30:31], s[2:3], v[150:151] op_sel_hi:[1,0,1]
	s_add_i32 s2, s0, 5
	v_readlane_b32 s2, v188, s2
	s_waitcnt vmcnt(20)
	v_cvt_scalef32_pk32_f32_fp6 v[0:31], v[50:55], 1.0
	v_pk_fma_f32 v[50:51], v[0:1], s[2:3], v[62:63] op_sel_hi:[1,0,1]
	v_pk_fma_f32 v[52:53], v[2:3], s[2:3], v[64:65] op_sel_hi:[1,0,1]
	v_pk_fma_f32 v[54:55], v[4:5], s[2:3], v[66:67] op_sel_hi:[1,0,1]
	v_pk_fma_f32 v[62:63], v[6:7], s[2:3], v[164:165] op_sel_hi:[1,0,1]
	v_pk_fma_f32 v[64:65], v[8:9], s[2:3], v[166:167] op_sel_hi:[1,0,1]
	v_pk_fma_f32 v[66:67], v[10:11], s[2:3], v[168:169] op_sel_hi:[1,0,1]
	v_pk_fma_f32 v[164:165], v[12:13], s[2:3], v[170:171] op_sel_hi:[1,0,1]
	v_pk_fma_f32 v[166:167], v[14:15], s[2:3], v[172:173] op_sel_hi:[1,0,1]
	v_pk_fma_f32 v[168:169], v[16:17], s[2:3], v[174:175] op_sel_hi:[1,0,1]
	v_pk_fma_f32 v[162:163], v[18:19], s[2:3], v[162:163] op_sel_hi:[1,0,1]
	v_pk_fma_f32 v[160:161], v[20:21], s[2:3], v[160:161] op_sel_hi:[1,0,1]
	v_pk_fma_f32 v[158:159], v[22:23], s[2:3], v[158:159] op_sel_hi:[1,0,1]
	v_pk_fma_f32 v[156:157], v[24:25], s[2:3], v[156:157] op_sel_hi:[1,0,1]
	v_pk_fma_f32 v[154:155], v[26:27], s[2:3], v[154:155] op_sel_hi:[1,0,1]
	v_pk_fma_f32 v[152:153], v[28:29], s[2:3], v[152:153] op_sel_hi:[1,0,1]
	v_pk_fma_f32 v[150:151], v[30:31], s[2:3], v[150:151] op_sel_hi:[1,0,1]
	s_add_i32 s2, s0, 6
	v_readlane_b32 s2, v188, s2
	s_waitcnt vmcnt(18)
	v_cvt_scalef32_pk32_f32_fp6 v[0:31], v[38:43], 1.0
	v_pk_fma_f32 v[38:39], v[0:1], s[2:3], v[50:51] op_sel_hi:[1,0,1]
	v_pk_fma_f32 v[40:41], v[2:3], s[2:3], v[52:53] op_sel_hi:[1,0,1]
	v_pk_fma_f32 v[42:43], v[4:5], s[2:3], v[54:55] op_sel_hi:[1,0,1]
	v_pk_fma_f32 v[50:51], v[6:7], s[2:3], v[62:63] op_sel_hi:[1,0,1]
	v_pk_fma_f32 v[52:53], v[8:9], s[2:3], v[64:65] op_sel_hi:[1,0,1]
	v_pk_fma_f32 v[54:55], v[10:11], s[2:3], v[66:67] op_sel_hi:[1,0,1]
	v_pk_fma_f32 v[62:63], v[12:13], s[2:3], v[164:165] op_sel_hi:[1,0,1]
	v_pk_fma_f32 v[64:65], v[14:15], s[2:3], v[166:167] op_sel_hi:[1,0,1]
	v_pk_fma_f32 v[66:67], v[16:17], s[2:3], v[168:169] op_sel_hi:[1,0,1]
	v_pk_fma_f32 v[162:163], v[18:19], s[2:3], v[162:163] op_sel_hi:[1,0,1]
	v_pk_fma_f32 v[160:161], v[20:21], s[2:3], v[160:161] op_sel_hi:[1,0,1]
	v_pk_fma_f32 v[158:159], v[22:23], s[2:3], v[158:159] op_sel_hi:[1,0,1]
	v_pk_fma_f32 v[156:157], v[24:25], s[2:3], v[156:157] op_sel_hi:[1,0,1]
	v_pk_fma_f32 v[154:155], v[26:27], s[2:3], v[154:155] op_sel_hi:[1,0,1]
	v_pk_fma_f32 v[152:153], v[28:29], s[2:3], v[152:153] op_sel_hi:[1,0,1]
	v_pk_fma_f32 v[150:151], v[30:31], s[2:3], v[150:151] op_sel_hi:[1,0,1]
	s_add_i32 s2, s0, 7
	v_readlane_b32 s2, v188, s2
	s_waitcnt vmcnt(16)
	v_cvt_scalef32_pk32_f32_fp6 v[0:31], v[32:37], 1.0
	v_pk_fma_f32 v[164:165], v[0:1], s[2:3], v[38:39] op_sel_hi:[1,0,1]
	v_pk_fma_f32 v[166:167], v[2:3], s[2:3], v[40:41] op_sel_hi:[1,0,1]
	v_pk_fma_f32 v[168:169], v[4:5], s[2:3], v[42:43] op_sel_hi:[1,0,1]
	v_pk_fma_f32 v[170:171], v[6:7], s[2:3], v[50:51] op_sel_hi:[1,0,1]
	v_pk_fma_f32 v[172:173], v[8:9], s[2:3], v[52:53] op_sel_hi:[1,0,1]
	v_pk_fma_f32 v[174:175], v[10:11], s[2:3], v[54:55] op_sel_hi:[1,0,1]
	v_pk_fma_f32 v[176:177], v[12:13], s[2:3], v[62:63] op_sel_hi:[1,0,1]
	v_pk_fma_f32 v[178:179], v[14:15], s[2:3], v[64:65] op_sel_hi:[1,0,1]
	v_pk_fma_f32 v[180:181], v[16:17], s[2:3], v[66:67] op_sel_hi:[1,0,1]
	v_pk_fma_f32 v[162:163], v[18:19], s[2:3], v[162:163] op_sel_hi:[1,0,1]
	v_pk_fma_f32 v[160:161], v[20:21], s[2:3], v[160:161] op_sel_hi:[1,0,1]
	v_pk_fma_f32 v[158:159], v[22:23], s[2:3], v[158:159] op_sel_hi:[1,0,1]
	v_pk_fma_f32 v[156:157], v[24:25], s[2:3], v[156:157] op_sel_hi:[1,0,1]
	v_pk_fma_f32 v[154:155], v[26:27], s[2:3], v[154:155] op_sel_hi:[1,0,1]
	v_pk_fma_f32 v[152:153], v[28:29], s[2:3], v[152:153] op_sel_hi:[1,0,1]
	v_pk_fma_f32 v[150:151], v[30:31], s[2:3], v[150:151] op_sel_hi:[1,0,1]
	s_cmp_lt_u32 s0, 48
	s_cselect_b64 s[2:3], -1, 0
	s_add_i32 s100, s0, 17
	s_add_i32 s101, s0, 18
	v_cndmask_b32_e64 v0, v241, v240, s[2:3]
	s_add_i32 s2, s0, 16
	s_nop 0
	v_readlane_b32 s2, v0, s2
	s_add_i32 s3, s0, 19
	v_readlane_b32 s100, v0, s100
	v_readlane_b32 s101, v0, s101
	v_readlane_b32 s3, v0, s3
	s_nop 1
	buffer_load_dwordx4 v[62:65], v129, s[44:47], s2 offen
	buffer_load_dwordx2 v[66:67], v210, s[44:47], s2 offen
	buffer_load_dwordx4 v[50:53], v129, s[44:47], s100 offen
	buffer_load_dwordx2 v[54:55], v210, s[44:47], s100 offen
	buffer_load_dwordx4 v[38:41], v129, s[44:47], s101 offen
	buffer_load_dwordx2 v[42:43], v210, s[44:47], s101 offen
	buffer_load_dwordx4 v[32:35], v129, s[44:47], s3 offen
	buffer_load_dwordx2 v[36:37], v210, s[44:47], s3 offen
	v_cndmask_b32_e32 v188, v131, v211, vcc
	s_waitcnt vmcnt(22)
	v_cvt_scalef32_pk32_f32_fp6 v[0:31], v[98:103], 1.0
	v_readlane_b32 s2, v188, s6
	s_nop 1
	v_pk_fma_f32 v[98:99], v[0:1], s[2:3], v[164:165] op_sel_hi:[1,0,1]
	v_pk_fma_f32 v[100:101], v[2:3], s[2:3], v[166:167] op_sel_hi:[1,0,1]
	v_pk_fma_f32 v[102:103], v[4:5], s[2:3], v[168:169] op_sel_hi:[1,0,1]
	v_pk_fma_f32 v[164:165], v[6:7], s[2:3], v[170:171] op_sel_hi:[1,0,1]
	v_pk_fma_f32 v[166:167], v[8:9], s[2:3], v[172:173] op_sel_hi:[1,0,1]
	v_pk_fma_f32 v[168:169], v[10:11], s[2:3], v[174:175] op_sel_hi:[1,0,1]
	v_pk_fma_f32 v[170:171], v[12:13], s[2:3], v[176:177] op_sel_hi:[1,0,1]
	v_pk_fma_f32 v[172:173], v[14:15], s[2:3], v[178:179] op_sel_hi:[1,0,1]
	v_pk_fma_f32 v[174:175], v[16:17], s[2:3], v[180:181] op_sel_hi:[1,0,1]
	v_pk_fma_f32 v[162:163], v[18:19], s[2:3], v[162:163] op_sel_hi:[1,0,1]
	v_pk_fma_f32 v[160:161], v[20:21], s[2:3], v[160:161] op_sel_hi:[1,0,1]
	v_pk_fma_f32 v[158:159], v[22:23], s[2:3], v[158:159] op_sel_hi:[1,0,1]
	v_pk_fma_f32 v[156:157], v[24:25], s[2:3], v[156:157] op_sel_hi:[1,0,1]
	v_pk_fma_f32 v[154:155], v[26:27], s[2:3], v[154:155] op_sel_hi:[1,0,1]
	v_pk_fma_f32 v[152:153], v[28:29], s[2:3], v[152:153] op_sel_hi:[1,0,1]
	v_pk_fma_f32 v[150:151], v[30:31], s[2:3], v[150:151] op_sel_hi:[1,0,1]
	v_readlane_b32 s2, v188, s5
	s_waitcnt vmcnt(20)
	v_cvt_scalef32_pk32_f32_fp6 v[0:31], v[92:97], 1.0
	v_pk_fma_f32 v[92:93], v[0:1], s[2:3], v[98:99] op_sel_hi:[1,0,1]
	v_pk_fma_f32 v[94:95], v[2:3], s[2:3], v[100:101] op_sel_hi:[1,0,1]
	v_pk_fma_f32 v[96:97], v[4:5], s[2:3], v[102:103] op_sel_hi:[1,0,1]
	v_pk_fma_f32 v[98:99], v[6:7], s[2:3], v[164:165] op_sel_hi:[1,0,1]
	v_pk_fma_f32 v[100:101], v[8:9], s[2:3], v[166:167] op_sel_hi:[1,0,1]
	v_pk_fma_f32 v[102:103], v[10:11], s[2:3], v[168:169] op_sel_hi:[1,0,1]
	v_pk_fma_f32 v[164:165], v[12:13], s[2:3], v[170:171] op_sel_hi:[1,0,1]
	v_pk_fma_f32 v[166:167], v[14:15], s[2:3], v[172:173] op_sel_hi:[1,0,1]
	v_pk_fma_f32 v[168:169], v[16:17], s[2:3], v[174:175] op_sel_hi:[1,0,1]
	v_pk_fma_f32 v[162:163], v[18:19], s[2:3], v[162:163] op_sel_hi:[1,0,1]
	v_pk_fma_f32 v[160:161], v[20:21], s[2:3], v[160:161] op_sel_hi:[1,0,1]
	v_pk_fma_f32 v[158:159], v[22:23], s[2:3], v[158:159] op_sel_hi:[1,0,1]
	v_pk_fma_f32 v[156:157], v[24:25], s[2:3], v[156:157] op_sel_hi:[1,0,1]
	v_pk_fma_f32 v[154:155], v[26:27], s[2:3], v[154:155] op_sel_hi:[1,0,1]
	v_pk_fma_f32 v[152:153], v[28:29], s[2:3], v[152:153] op_sel_hi:[1,0,1]
	v_pk_fma_f32 v[150:151], v[30:31], s[2:3], v[150:151] op_sel_hi:[1,0,1]
	v_readlane_b32 s2, v188, s4
	s_waitcnt vmcnt(18)
	v_cvt_scalef32_pk32_f32_fp6 v[0:31], v[86:91], 1.0
	v_pk_fma_f32 v[86:87], v[0:1], s[2:3], v[92:93] op_sel_hi:[1,0,1]
	v_pk_fma_f32 v[88:89], v[2:3], s[2:3], v[94:95] op_sel_hi:[1,0,1]
	v_pk_fma_f32 v[90:91], v[4:5], s[2:3], v[96:97] op_sel_hi:[1,0,1]
	v_pk_fma_f32 v[92:93], v[6:7], s[2:3], v[98:99] op_sel_hi:[1,0,1]
	v_pk_fma_f32 v[94:95], v[8:9], s[2:3], v[100:101] op_sel_hi:[1,0,1]
	v_pk_fma_f32 v[96:97], v[10:11], s[2:3], v[102:103] op_sel_hi:[1,0,1]
	v_pk_fma_f32 v[98:99], v[12:13], s[2:3], v[164:165] op_sel_hi:[1,0,1]
	v_pk_fma_f32 v[100:101], v[14:15], s[2:3], v[166:167] op_sel_hi:[1,0,1]
	v_pk_fma_f32 v[102:103], v[16:17], s[2:3], v[168:169] op_sel_hi:[1,0,1]
	v_pk_fma_f32 v[162:163], v[18:19], s[2:3], v[162:163] op_sel_hi:[1,0,1]
	v_pk_fma_f32 v[160:161], v[20:21], s[2:3], v[160:161] op_sel_hi:[1,0,1]
	v_pk_fma_f32 v[158:159], v[22:23], s[2:3], v[158:159] op_sel_hi:[1,0,1]
	v_pk_fma_f32 v[156:157], v[24:25], s[2:3], v[156:157] op_sel_hi:[1,0,1]
	v_pk_fma_f32 v[154:155], v[26:27], s[2:3], v[154:155] op_sel_hi:[1,0,1]
	v_pk_fma_f32 v[152:153], v[28:29], s[2:3], v[152:153] op_sel_hi:[1,0,1]
	v_pk_fma_f32 v[150:151], v[30:31], s[2:3], v[150:151] op_sel_hi:[1,0,1]
	v_readlane_b32 s2, v188, s1
	s_waitcnt vmcnt(16)
	v_cvt_scalef32_pk32_f32_fp6 v[0:31], v[80:85], 1.0
	v_pk_fma_f32 v[180:181], v[0:1], s[2:3], v[86:87] op_sel_hi:[1,0,1]
	v_pk_fma_f32 v[178:179], v[2:3], s[2:3], v[88:89] op_sel_hi:[1,0,1]
	v_pk_fma_f32 v[176:177], v[4:5], s[2:3], v[90:91] op_sel_hi:[1,0,1]
	v_pk_fma_f32 v[174:175], v[6:7], s[2:3], v[92:93] op_sel_hi:[1,0,1]
	v_pk_fma_f32 v[172:173], v[8:9], s[2:3], v[94:95] op_sel_hi:[1,0,1]
	v_pk_fma_f32 v[170:171], v[10:11], s[2:3], v[96:97] op_sel_hi:[1,0,1]
	v_pk_fma_f32 v[168:169], v[12:13], s[2:3], v[98:99] op_sel_hi:[1,0,1]
	v_pk_fma_f32 v[166:167], v[14:15], s[2:3], v[100:101] op_sel_hi:[1,0,1]
	v_pk_fma_f32 v[164:165], v[16:17], s[2:3], v[102:103] op_sel_hi:[1,0,1]
	v_pk_fma_f32 v[162:163], v[18:19], s[2:3], v[162:163] op_sel_hi:[1,0,1]
	v_pk_fma_f32 v[160:161], v[20:21], s[2:3], v[160:161] op_sel_hi:[1,0,1]
	v_pk_fma_f32 v[158:159], v[22:23], s[2:3], v[158:159] op_sel_hi:[1,0,1]
	v_pk_fma_f32 v[156:157], v[24:25], s[2:3], v[156:157] op_sel_hi:[1,0,1]
	v_pk_fma_f32 v[154:155], v[26:27], s[2:3], v[154:155] op_sel_hi:[1,0,1]
	v_pk_fma_f32 v[152:153], v[28:29], s[2:3], v[152:153] op_sel_hi:[1,0,1]
	v_pk_fma_f32 v[150:151], v[30:31], s[2:3], v[150:151] op_sel_hi:[1,0,1]
	s_cmpk_lt_u32 s0, 0x64
	s_mov_b32 s0, s7
	s_cbranch_scc1 .LBB0_1139
	v_readlane_b32 s0, v131, 56
	s_waitcnt vmcnt(14)
	v_cvt_scalef32_pk32_f32_fp6 v[0:31], v[74:79], 1.0
	v_pk_fma_f32 v[74:75], v[0:1], s[0:1], v[180:181] op_sel_hi:[1,0,1]
	v_pk_fma_f32 v[76:77], v[2:3], s[0:1], v[178:179] op_sel_hi:[1,0,1]
	v_pk_fma_f32 v[78:79], v[4:5], s[0:1], v[176:177] op_sel_hi:[1,0,1]
	v_pk_fma_f32 v[80:81], v[6:7], s[0:1], v[174:175] op_sel_hi:[1,0,1]
	v_pk_fma_f32 v[82:83], v[8:9], s[0:1], v[172:173] op_sel_hi:[1,0,1]
	v_pk_fma_f32 v[84:85], v[10:11], s[0:1], v[170:171] op_sel_hi:[1,0,1]
	v_pk_fma_f32 v[86:87], v[12:13], s[0:1], v[168:169] op_sel_hi:[1,0,1]
	v_pk_fma_f32 v[88:89], v[14:15], s[0:1], v[166:167] op_sel_hi:[1,0,1]
	v_pk_fma_f32 v[90:91], v[16:17], s[0:1], v[164:165] op_sel_hi:[1,0,1]
	v_pk_fma_f32 v[92:93], v[18:19], s[0:1], v[162:163] op_sel_hi:[1,0,1]
	v_pk_fma_f32 v[94:95], v[20:21], s[0:1], v[160:161] op_sel_hi:[1,0,1]
	v_pk_fma_f32 v[96:97], v[22:23], s[0:1], v[158:159] op_sel_hi:[1,0,1]
	v_pk_fma_f32 v[98:99], v[24:25], s[0:1], v[156:157] op_sel_hi:[1,0,1]
	v_pk_fma_f32 v[100:101], v[26:27], s[0:1], v[154:155] op_sel_hi:[1,0,1]
	v_pk_fma_f32 v[102:103], v[28:29], s[0:1], v[152:153] op_sel_hi:[1,0,1]
	v_pk_fma_f32 v[150:151], v[30:31], s[0:1], v[150:151] op_sel_hi:[1,0,1]
	v_readlane_b32 s0, v131, 57
	s_waitcnt vmcnt(12)
	v_cvt_scalef32_pk32_f32_fp6 v[0:31], v[68:73], 1.0
	v_pk_fma_f32 v[68:69], v[0:1], s[0:1], v[74:75] op_sel_hi:[1,0,1]
	v_pk_fma_f32 v[70:71], v[2:3], s[0:1], v[76:77] op_sel_hi:[1,0,1]
	v_pk_fma_f32 v[72:73], v[4:5], s[0:1], v[78:79] op_sel_hi:[1,0,1]
	v_pk_fma_f32 v[74:75], v[6:7], s[0:1], v[80:81] op_sel_hi:[1,0,1]
	v_pk_fma_f32 v[76:77], v[8:9], s[0:1], v[82:83] op_sel_hi:[1,0,1]
	v_pk_fma_f32 v[78:79], v[10:11], s[0:1], v[84:85] op_sel_hi:[1,0,1]
	v_pk_fma_f32 v[80:81], v[12:13], s[0:1], v[86:87] op_sel_hi:[1,0,1]
	v_pk_fma_f32 v[82:83], v[14:15], s[0:1], v[88:89] op_sel_hi:[1,0,1]
	v_pk_fma_f32 v[84:85], v[16:17], s[0:1], v[90:91] op_sel_hi:[1,0,1]
	v_pk_fma_f32 v[86:87], v[18:19], s[0:1], v[92:93] op_sel_hi:[1,0,1]
	v_pk_fma_f32 v[88:89], v[20:21], s[0:1], v[94:95] op_sel_hi:[1,0,1]
	v_pk_fma_f32 v[90:91], v[22:23], s[0:1], v[96:97] op_sel_hi:[1,0,1]
	v_pk_fma_f32 v[92:93], v[24:25], s[0:1], v[98:99] op_sel_hi:[1,0,1]
	v_pk_fma_f32 v[94:95], v[26:27], s[0:1], v[100:101] op_sel_hi:[1,0,1]
	v_pk_fma_f32 v[96:97], v[28:29], s[0:1], v[102:103] op_sel_hi:[1,0,1]
	v_pk_fma_f32 v[98:99], v[30:31], s[0:1], v[150:151] op_sel_hi:[1,0,1]
	v_readlane_b32 s0, v131, 58
	s_waitcnt vmcnt(10)
	v_cvt_scalef32_pk32_f32_fp6 v[0:31], v[56:61], 1.0
	v_pk_fma_f32 v[56:57], v[0:1], s[0:1], v[68:69] op_sel_hi:[1,0,1]
	v_pk_fma_f32 v[58:59], v[2:3], s[0:1], v[70:71] op_sel_hi:[1,0,1]
	v_pk_fma_f32 v[60:61], v[4:5], s[0:1], v[72:73] op_sel_hi:[1,0,1]
	v_pk_fma_f32 v[68:69], v[6:7], s[0:1], v[74:75] op_sel_hi:[1,0,1]
	v_pk_fma_f32 v[70:71], v[8:9], s[0:1], v[76:77] op_sel_hi:[1,0,1]
	v_pk_fma_f32 v[72:73], v[10:11], s[0:1], v[78:79] op_sel_hi:[1,0,1]
	v_pk_fma_f32 v[74:75], v[12:13], s[0:1], v[80:81] op_sel_hi:[1,0,1]
	v_pk_fma_f32 v[76:77], v[14:15], s[0:1], v[82:83] op_sel_hi:[1,0,1]
	v_pk_fma_f32 v[78:79], v[16:17], s[0:1], v[84:85] op_sel_hi:[1,0,1]
	v_pk_fma_f32 v[80:81], v[18:19], s[0:1], v[86:87] op_sel_hi:[1,0,1]
	v_pk_fma_f32 v[82:83], v[20:21], s[0:1], v[88:89] op_sel_hi:[1,0,1]
	v_pk_fma_f32 v[84:85], v[22:23], s[0:1], v[90:91] op_sel_hi:[1,0,1]
	v_pk_fma_f32 v[86:87], v[24:25], s[0:1], v[92:93] op_sel_hi:[1,0,1]
	v_pk_fma_f32 v[88:89], v[26:27], s[0:1], v[94:95] op_sel_hi:[1,0,1]
	v_pk_fma_f32 v[90:91], v[28:29], s[0:1], v[96:97] op_sel_hi:[1,0,1]
	v_pk_fma_f32 v[92:93], v[30:31], s[0:1], v[98:99] op_sel_hi:[1,0,1]
	v_readlane_b32 s0, v131, 59
	s_waitcnt vmcnt(8)
	v_cvt_scalef32_pk32_f32_fp6 v[0:31], v[44:49], 1.0
	v_pk_fma_f32 v[46:47], v[2:3], s[0:1], v[58:59] op_sel_hi:[1,0,1]
	v_pk_fma_f32 v[44:45], v[0:1], s[0:1], v[56:57] op_sel_hi:[1,0,1]
	v_pk_fma_f32 v[48:49], v[4:5], s[0:1], v[60:61] op_sel_hi:[1,0,1]
	v_pk_fma_f32 v[56:57], v[6:7], s[0:1], v[68:69] op_sel_hi:[1,0,1]
	v_pk_fma_f32 v[58:59], v[8:9], s[0:1], v[70:71] op_sel_hi:[1,0,1]
	v_pk_fma_f32 v[60:61], v[10:11], s[0:1], v[72:73] op_sel_hi:[1,0,1]
	v_pk_fma_f32 v[68:69], v[12:13], s[0:1], v[74:75] op_sel_hi:[1,0,1]
	v_pk_fma_f32 v[70:71], v[14:15], s[0:1], v[76:77] op_sel_hi:[1,0,1]
	v_pk_fma_f32 v[72:73], v[16:17], s[0:1], v[78:79] op_sel_hi:[1,0,1]
	v_pk_fma_f32 v[74:75], v[18:19], s[0:1], v[80:81] op_sel_hi:[1,0,1]
	v_pk_fma_f32 v[76:77], v[20:21], s[0:1], v[82:83] op_sel_hi:[1,0,1]
	v_pk_fma_f32 v[78:79], v[22:23], s[0:1], v[84:85] op_sel_hi:[1,0,1]
	v_pk_fma_f32 v[80:81], v[24:25], s[0:1], v[86:87] op_sel_hi:[1,0,1]
	v_pk_fma_f32 v[82:83], v[26:27], s[0:1], v[88:89] op_sel_hi:[1,0,1]
	v_pk_fma_f32 v[84:85], v[28:29], s[0:1], v[90:91] op_sel_hi:[1,0,1]
	v_pk_fma_f32 v[86:87], v[30:31], s[0:1], v[92:93] op_sel_hi:[1,0,1]
	v_readlane_b32 s0, v131, 60
	s_waitcnt vmcnt(6)
	v_cvt_scalef32_pk32_f32_fp6 v[0:31], v[62:67], 1.0
	v_pk_fma_f32 v[44:45], v[0:1], s[0:1], v[44:45] op_sel_hi:[1,0,1]
	v_pk_fma_f32 v[46:47], v[2:3], s[0:1], v[46:47] op_sel_hi:[1,0,1]
	v_pk_fma_f32 v[48:49], v[4:5], s[0:1], v[48:49] op_sel_hi:[1,0,1]
	v_pk_fma_f32 v[56:57], v[6:7], s[0:1], v[56:57] op_sel_hi:[1,0,1]
	v_pk_fma_f32 v[58:59], v[8:9], s[0:1], v[58:59] op_sel_hi:[1,0,1]
	v_pk_fma_f32 v[60:61], v[10:11], s[0:1], v[60:61] op_sel_hi:[1,0,1]
	v_pk_fma_f32 v[62:63], v[12:13], s[0:1], v[68:69] op_sel_hi:[1,0,1]
	v_pk_fma_f32 v[64:65], v[14:15], s[0:1], v[70:71] op_sel_hi:[1,0,1]
	v_pk_fma_f32 v[66:67], v[16:17], s[0:1], v[72:73] op_sel_hi:[1,0,1]
	v_pk_fma_f32 v[68:69], v[18:19], s[0:1], v[74:75] op_sel_hi:[1,0,1]
	v_pk_fma_f32 v[70:71], v[20:21], s[0:1], v[76:77] op_sel_hi:[1,0,1]
	v_pk_fma_f32 v[72:73], v[22:23], s[0:1], v[78:79] op_sel_hi:[1,0,1]
	v_pk_fma_f32 v[74:75], v[24:25], s[0:1], v[80:81] op_sel_hi:[1,0,1]
	v_pk_fma_f32 v[76:77], v[26:27], s[0:1], v[82:83] op_sel_hi:[1,0,1]
	v_pk_fma_f32 v[78:79], v[28:29], s[0:1], v[84:85] op_sel_hi:[1,0,1]
	v_pk_fma_f32 v[80:81], v[30:31], s[0:1], v[86:87] op_sel_hi:[1,0,1]
	v_readlane_b32 s0, v131, 61
	s_waitcnt vmcnt(4)
	v_cvt_scalef32_pk32_f32_fp6 v[0:31], v[50:55], 1.0
	v_pk_fma_f32 v[44:45], v[0:1], s[0:1], v[44:45] op_sel_hi:[1,0,1]
	v_pk_fma_f32 v[46:47], v[2:3], s[0:1], v[46:47] op_sel_hi:[1,0,1]
	v_pk_fma_f32 v[48:49], v[4:5], s[0:1], v[48:49] op_sel_hi:[1,0,1]
	v_pk_fma_f32 v[50:51], v[6:7], s[0:1], v[56:57] op_sel_hi:[1,0,1]
	v_pk_fma_f32 v[52:53], v[8:9], s[0:1], v[58:59] op_sel_hi:[1,0,1]
	v_pk_fma_f32 v[54:55], v[10:11], s[0:1], v[60:61] op_sel_hi:[1,0,1]
	v_pk_fma_f32 v[56:57], v[12:13], s[0:1], v[62:63] op_sel_hi:[1,0,1]
	v_pk_fma_f32 v[58:59], v[14:15], s[0:1], v[64:65] op_sel_hi:[1,0,1]
	v_pk_fma_f32 v[60:61], v[16:17], s[0:1], v[66:67] op_sel_hi:[1,0,1]
	v_pk_fma_f32 v[62:63], v[18:19], s[0:1], v[68:69] op_sel_hi:[1,0,1]
	v_pk_fma_f32 v[64:65], v[20:21], s[0:1], v[70:71] op_sel_hi:[1,0,1]
	v_pk_fma_f32 v[66:67], v[22:23], s[0:1], v[72:73] op_sel_hi:[1,0,1]
	v_pk_fma_f32 v[68:69], v[24:25], s[0:1], v[74:75] op_sel_hi:[1,0,1]
	v_pk_fma_f32 v[70:71], v[26:27], s[0:1], v[76:77] op_sel_hi:[1,0,1]
	v_pk_fma_f32 v[72:73], v[28:29], s[0:1], v[78:79] op_sel_hi:[1,0,1]
	v_pk_fma_f32 v[74:75], v[30:31], s[0:1], v[80:81] op_sel_hi:[1,0,1]
	v_readlane_b32 s0, v131, 62
	s_waitcnt vmcnt(2)
	v_cvt_scalef32_pk32_f32_fp6 v[0:31], v[38:43], 1.0
	v_pk_fma_f32 v[38:39], v[0:1], s[0:1], v[44:45] op_sel_hi:[1,0,1]
	v_pk_fma_f32 v[40:41], v[2:3], s[0:1], v[46:47] op_sel_hi:[1,0,1]
	v_pk_fma_f32 v[42:43], v[4:5], s[0:1], v[48:49] op_sel_hi:[1,0,1]
	v_pk_fma_f32 v[44:45], v[6:7], s[0:1], v[50:51] op_sel_hi:[1,0,1]
	v_pk_fma_f32 v[46:47], v[8:9], s[0:1], v[52:53] op_sel_hi:[1,0,1]
	v_pk_fma_f32 v[48:49], v[10:11], s[0:1], v[54:55] op_sel_hi:[1,0,1]
	v_pk_fma_f32 v[50:51], v[12:13], s[0:1], v[56:57] op_sel_hi:[1,0,1]
	v_pk_fma_f32 v[52:53], v[14:15], s[0:1], v[58:59] op_sel_hi:[1,0,1]
	v_pk_fma_f32 v[54:55], v[16:17], s[0:1], v[60:61] op_sel_hi:[1,0,1]
	v_pk_fma_f32 v[56:57], v[18:19], s[0:1], v[62:63] op_sel_hi:[1,0,1]
	v_pk_fma_f32 v[58:59], v[20:21], s[0:1], v[64:65] op_sel_hi:[1,0,1]
	v_pk_fma_f32 v[62:63], v[22:23], s[0:1], v[66:67] op_sel_hi:[1,0,1]
	v_pk_fma_f32 v[64:65], v[24:25], s[0:1], v[68:69] op_sel_hi:[1,0,1]
	v_pk_fma_f32 v[66:67], v[26:27], s[0:1], v[70:71] op_sel_hi:[1,0,1]
	v_pk_fma_f32 v[68:69], v[28:29], s[0:1], v[72:73] op_sel_hi:[1,0,1]
	v_pk_fma_f32 v[70:71], v[30:31], s[0:1], v[74:75] op_sel_hi:[1,0,1]
	v_readlane_b32 s0, v131, 63
	s_waitcnt vmcnt(0)
	v_cvt_scalef32_pk32_f32_fp6 v[0:31], v[32:37], 1.0
	v_pk_fma_f32 v[34:35], v[0:1], s[0:1], v[38:39] op_sel_hi:[1,0,1]
	v_pk_fma_f32 v[32:33], v[2:3], s[0:1], v[40:41] op_sel_hi:[1,0,1]
	v_pk_fma_f32 v[38:39], v[4:5], s[0:1], v[42:43] op_sel_hi:[1,0,1]
	v_pk_fma_f32 v[36:37], v[6:7], s[0:1], v[44:45] op_sel_hi:[1,0,1]
	v_pk_fma_f32 v[42:43], v[8:9], s[0:1], v[46:47] op_sel_hi:[1,0,1]
	v_pk_fma_f32 v[40:41], v[10:11], s[0:1], v[48:49] op_sel_hi:[1,0,1]
	v_pk_fma_f32 v[48:49], v[12:13], s[0:1], v[50:51] op_sel_hi:[1,0,1]
	v_pk_fma_f32 v[46:47], v[14:15], s[0:1], v[52:53] op_sel_hi:[1,0,1]
	v_pk_fma_f32 v[50:51], v[18:19], s[0:1], v[56:57] op_sel_hi:[1,0,1]
	v_pk_fma_f32 v[54:55], v[16:17], s[0:1], v[54:55] op_sel_hi:[1,0,1]
	v_pk_fma_f32 v[60:61], v[20:21], s[0:1], v[58:59] op_sel_hi:[1,0,1]
	v_pk_fma_f32 v[56:57], v[22:23], s[0:1], v[62:63] op_sel_hi:[1,0,1]
	v_pk_fma_f32 v[44:45], v[24:25], s[0:1], v[64:65] op_sel_hi:[1,0,1]
	v_pk_fma_f32 v[64:65], v[26:27], s[0:1], v[66:67] op_sel_hi:[1,0,1]
	v_pk_fma_f32 v[18:19], v[28:29], s[0:1], v[68:69] op_sel_hi:[1,0,1]
	v_pk_fma_f32 v[24:25], v[30:31], s[0:1], v[70:71] op_sel_hi:[1,0,1]
	s_lshr_b32 s0, s58, 12
	s_ashr_i32 s59, s58, 31
	s_mul_i32 s4, s0, 0x3000
	s_lshl_b64 s[0:1], s[58:59], 12
	s_add_u32 s2, s71, s0
	v_lshlrev_b32_e32 v12, 2, v148
	s_addc_u32 s3, s74, s1
	v_ashrrev_i32_e32 v13, 31, v12
	v_lshlrev_b32_e32 v63, 3, v148
	v_lshl_add_u64 v[14:15], v[12:13], 1, s[2:3]
	v_add3_u32 v62, v201, s4, v63
	global_load_dwordx2 v[16:17], v[14:15], off
	ds_read2st64_b64 v[0:3], v62 offset1:1
	global_load_dwordx2 v[20:21], v[14:15], off offset:512
	global_load_dwordx2 v[22:23], v[14:15], off offset:1024
	ds_read2st64_b64 v[4:7], v62 offset0:2 offset1:3
	global_load_dwordx2 v[52:53], v[14:15], off offset:1536
	global_load_dwordx2 v[58:59], v[14:15], off offset:2048
	ds_read2st64_b64 v[8:11], v62 offset0:4 offset1:5
	global_load_dwordx2 v[66:67], v[14:15], off offset:2560
	global_load_dwordx2 v[68:69], v[14:15], off offset:3072
	global_load_dwordx2 v[26:27], v[14:15], off offset:3584
	ds_read2st64_b64 v[28:31], v62 offset0:6 offset1:7
	s_lshl_b64 s[2:3], s[58:59], 13
	s_add_u32 s4, s16, s2
	s_addc_u32 s5, s17, s3
	s_and_b64 vcc, exec, s[54:55]
	s_waitcnt lgkmcnt(0)
	v_lshlrev_b32_e32 v72, 16, v30
	v_and_b32_e32 v73, 0xffff0000, v30
	v_lshlrev_b32_e32 v30, 16, v31
	v_and_b32_e32 v31, 0xffff0000, v31
	v_pk_mul_f32 v[24:25], v[24:25], v[30:31]
	v_lshlrev_b32_e32 v30, 16, v28
	v_and_b32_e32 v31, 0xffff0000, v28
	v_pk_mul_f32 v[30:31], v[44:45], v[30:31]
	v_lshlrev_b32_e32 v28, 16, v29
	v_and_b32_e32 v29, 0xffff0000, v29
	v_pk_mul_f32 v[28:29], v[64:65], v[28:29]
	v_pk_mul_f32 v[18:19], v[18:19], v[72:73]
	s_waitcnt vmcnt(0)
	v_lshlrev_b32_e32 v70, 16, v26
	v_and_b32_e32 v71, 0xffff0000, v26
	v_lshlrev_b32_e32 v26, 16, v27
	v_and_b32_e32 v27, 0xffff0000, v27
	v_pk_fma_f32 v[24:25], v[26:27], s[38:39], v[24:25] op_sel_hi:[1,0,1]
	v_lshlrev_b32_e32 v26, 16, v68
	v_and_b32_e32 v27, 0xffff0000, v68
	v_pk_fma_f32 v[26:27], v[26:27], s[38:39], v[30:31] op_sel_hi:[1,0,1]
	v_lshlrev_b32_e32 v30, 16, v69
	v_and_b32_e32 v31, 0xffff0000, v69
	v_pk_fma_f32 v[44:45], v[30:31], s[38:39], v[28:29] op_sel_hi:[1,0,1]
	v_lshlrev_b32_e32 v30, 16, v10
	v_and_b32_e32 v31, 0xffff0000, v10
	v_lshlrev_b32_e32 v28, 16, v66
	v_and_b32_e32 v29, 0xffff0000, v66
	v_pk_mul_f32 v[30:31], v[60:61], v[30:31]
	v_lshlrev_b32_e32 v10, 16, v11
	v_and_b32_e32 v11, 0xffff0000, v11
	v_pk_fma_f32 v[28:29], v[28:29], s[38:39], v[30:31] op_sel_hi:[1,0,1]
	v_lshlrev_b32_e32 v30, 16, v67
	v_and_b32_e32 v31, 0xffff0000, v67
	v_pk_mul_f32 v[10:11], v[56:57], v[10:11]
	v_lshlrev_b32_e32 v56, 16, v8
	v_and_b32_e32 v57, 0xffff0000, v8
	v_pk_fma_f32 v[10:11], v[30:31], s[38:39], v[10:11] op_sel_hi:[1,0,1]
	v_lshlrev_b32_e32 v30, 16, v58
	v_and_b32_e32 v31, 0xffff0000, v58
	v_pk_mul_f32 v[54:55], v[54:55], v[56:57]
	v_lshlrev_b32_e32 v8, 16, v9
	v_and_b32_e32 v9, 0xffff0000, v9
	v_pk_fma_f32 v[30:31], v[30:31], s[38:39], v[54:55] op_sel_hi:[1,0,1]
	v_lshlrev_b32_e32 v54, 16, v59
	v_and_b32_e32 v55, 0xffff0000, v59
	v_pk_mul_f32 v[8:9], v[50:51], v[8:9]
	v_lshlrev_b32_e32 v50, 16, v52
	v_pk_fma_f32 v[8:9], v[54:55], s[38:39], v[8:9] op_sel_hi:[1,0,1]
	v_lshlrev_b32_e32 v54, 16, v6
	v_and_b32_e32 v55, 0xffff0000, v6
	v_and_b32_e32 v51, 0xffff0000, v52
	v_pk_mul_f32 v[48:49], v[48:49], v[54:55]
	v_lshlrev_b32_e32 v6, 16, v7
	v_and_b32_e32 v7, 0xffff0000, v7
	v_pk_fma_f32 v[48:49], v[50:51], s[38:39], v[48:49] op_sel_hi:[1,0,1]
	v_lshlrev_b32_e32 v50, 16, v53
	v_and_b32_e32 v51, 0xffff0000, v53
	v_pk_mul_f32 v[6:7], v[46:47], v[6:7]
	v_lshlrev_b32_e32 v46, 16, v22
	v_pk_fma_f32 v[6:7], v[50:51], s[38:39], v[6:7] op_sel_hi:[1,0,1]
	v_lshlrev_b32_e32 v50, 16, v4
	v_and_b32_e32 v51, 0xffff0000, v4
	v_lshlrev_b32_e32 v4, 16, v5
	v_and_b32_e32 v5, 0xffff0000, v5
	v_and_b32_e32 v47, 0xffff0000, v22
	v_lshlrev_b32_e32 v22, 16, v23
	v_and_b32_e32 v23, 0xffff0000, v23
	v_pk_mul_f32 v[4:5], v[40:41], v[4:5]
	v_lshlrev_b32_e32 v40, 16, v2
	v_and_b32_e32 v41, 0xffff0000, v2
	v_pk_fma_f32 v[4:5], v[22:23], s[38:39], v[4:5] op_sel_hi:[1,0,1]
	v_lshlrev_b32_e32 v22, 16, v20
	v_and_b32_e32 v23, 0xffff0000, v20
	v_pk_mul_f32 v[38:39], v[38:39], v[40:41]
	v_lshlrev_b32_e32 v40, 16, v0
	v_and_b32_e32 v41, 0xffff0000, v0
	v_pk_fma_f32 v[22:23], v[22:23], s[38:39], v[38:39] op_sel_hi:[1,0,1]
	v_lshlrev_b32_e32 v38, 16, v16
	v_and_b32_e32 v39, 0xffff0000, v16
	v_pk_mul_f32 v[34:35], v[34:35], v[40:41]
	v_lshlrev_b32_e32 v16, 16, v17
	v_pk_fma_f32 v[34:35], v[38:39], s[38:39], v[34:35] op_sel_hi:[1,0,1]
	v_and_b32_e32 v17, 0xffff0000, v17
	v_add_f32_e32 v0, 0, v34
	v_add_f32_e32 v38, v35, v0
	v_lshlrev_b32_e32 v0, 16, v1
	v_and_b32_e32 v1, 0xffff0000, v1
	v_pk_mul_f32 v[0:1], v[32:33], v[0:1]
	v_lshlrev_b32_e32 v2, 16, v3
	v_pk_fma_f32 v[0:1], v[16:17], s[38:39], v[0:1] op_sel_hi:[1,0,1]
	v_and_b32_e32 v3, 0xffff0000, v3
	v_add_f32_e32 v16, v0, v38
	v_add_f32_e32 v16, v1, v16
	v_lshlrev_b32_e32 v20, 16, v21
	v_and_b32_e32 v21, 0xffff0000, v21
	v_pk_mul_f32 v[2:3], v[36:37], v[2:3]
	v_add_f32_e32 v16, v22, v16
	v_pk_fma_f32 v[2:3], v[20:21], s[38:39], v[2:3] op_sel_hi:[1,0,1]
	v_add_f32_e32 v16, v23, v16
	v_pk_mul_f32 v[42:43], v[42:43], v[50:51]
	v_add_f32_e32 v16, v2, v16
	v_pk_fma_f32 v[52:53], v[46:47], s[38:39], v[42:43] op_sel_hi:[1,0,1]
	v_add_f32_e32 v16, v3, v16
	v_add_f32_e32 v16, v52, v16
	v_add_f32_e32 v16, v53, v16
	v_add_f32_e32 v16, v4, v16
	v_add_f32_e32 v16, v5, v16
	v_add_f32_e32 v16, v48, v16
	v_add_f32_e32 v16, v49, v16
	v_add_f32_e32 v16, v6, v16
	v_add_f32_e32 v16, v7, v16
	v_add_f32_e32 v16, v30, v16
	v_add_f32_e32 v16, v31, v16
	v_add_f32_e32 v16, v8, v16
	v_add_f32_e32 v16, v9, v16
	v_add_f32_e32 v16, v28, v16
	v_add_f32_e32 v16, v29, v16
	v_add_f32_e32 v16, v10, v16
	v_add_f32_e32 v16, v11, v16
	v_add_f32_e32 v16, v26, v16
	v_add_f32_e32 v16, v27, v16
	v_add_f32_e32 v16, v44, v16
	v_pk_fma_f32 v[18:19], v[70:71], s[38:39], v[18:19] op_sel_hi:[1,0,1]
	v_add_f32_e32 v16, v45, v16
	v_add_f32_e32 v16, v18, v16
	v_add_f32_e32 v16, v19, v16
	v_add_f32_e32 v16, v24, v16
	v_add_f32_e32 v16, v25, v16
	v_mov_b32_e32 v17, v105
	v_add_u32_e32 v50, v202, v63
	v_add_f32_dpp v16, v16, v16 quad_perm:[1,0,3,2] row_mask:0xf bank_mask:0xf bound_ctrl:1
	v_add_u32_e32 v51, v203, v63
	ds_read_b64 v[20:21], v50
	ds_read_b64 v[36:37], v51
	v_add_f32_dpp v16, v16, v16 quad_perm:[2,3,0,1] row_mask:0xf bank_mask:0xf bound_ctrl:1
	s_waitcnt lgkmcnt(1)
	v_lshlrev_b32_e32 v54, 16, v20
	v_add_f32_dpp v16, v16, v16 row_half_mirror row_mask:0xf bank_mask:0xf bound_ctrl:1
	s_waitcnt lgkmcnt(0)
	v_lshlrev_b32_e32 v56, 16, v36
	v_and_b32_e32 v57, 0xffff0000, v36
	v_add_f32_dpp v16, v16, v16 row_mirror row_mask:0xf bank_mask:0xf bound_ctrl:1
	v_lshlrev_b32_e32 v60, 16, v37
	v_and_b32_e32 v61, 0xffff0000, v37
	v_mov_b32_dpp v17, v16 row_bcast:15 row_mask:0xa bank_mask:0xf
	v_add_f32_e32 v16, v16, v17
	v_mov_b32_e32 v17, v105
	v_and_b32_e32 v55, 0xffff0000, v20
	v_lshlrev_b32_e32 v58, 16, v21
	v_mov_b32_dpp v17, v16 row_bcast:31 row_mask:0xc bank_mask:0xf
	v_add_f32_e32 v16, v16, v17
	v_and_b32_e32 v59, 0xffff0000, v21
	v_readlane_b32 s2, v16, 63
	s_nop 1
	v_mul_f32_e32 v64, s2, v187
	v_pk_add_f32 v[66:67], v[34:35], v[64:65] op_sel_hi:[1,0] neg_lo:[0,1] neg_hi:[0,1]
	v_pk_add_f32 v[70:71], v[0:1], v[64:65] op_sel_hi:[1,0] neg_lo:[0,1] neg_hi:[0,1]
	v_pk_mul_f32 v[68:69], v[66:67], v[66:67]
	v_pk_mul_f32 v[0:1], v[70:71], v[70:71]
	v_add_f32_e32 v63, v68, v69
	v_pk_add_f32 v[46:47], v[22:23], v[64:65] op_sel_hi:[1,0] neg_lo:[0,1] neg_hi:[0,1]
	v_add_f32_e32 v0, v0, v63
	v_pk_mul_f32 v[72:73], v[46:47], v[46:47]
	v_add_f32_e32 v0, v1, v0
	v_pk_add_f32 v[42:43], v[2:3], v[64:65] op_sel_hi:[1,0] neg_lo:[0,1] neg_hi:[0,1]
	v_add_f32_e32 v0, v72, v0
	v_pk_mul_f32 v[2:3], v[42:43], v[42:43]
	v_add_f32_e32 v0, v73, v0
	v_pk_add_f32 v[40:41], v[52:53], v[64:65] op_sel_hi:[1,0] neg_lo:[0,1] neg_hi:[0,1]
	v_add_f32_e32 v0, v2, v0
	v_pk_mul_f32 v[52:53], v[40:41], v[40:41]
	v_add_f32_e32 v0, v3, v0
	v_pk_add_f32 v[22:23], v[4:5], v[64:65] op_sel_hi:[1,0] neg_lo:[0,1] neg_hi:[0,1]
	v_add_f32_e32 v0, v52, v0
	v_pk_mul_f32 v[4:5], v[22:23], v[22:23]
	v_add_f32_e32 v0, v53, v0
	v_pk_add_f32 v[38:39], v[48:49], v[64:65] op_sel_hi:[1,0] neg_lo:[0,1] neg_hi:[0,1]
	v_add_f32_e32 v0, v4, v0
	v_pk_mul_f32 v[48:49], v[38:39], v[38:39]
	v_add_f32_e32 v0, v5, v0
	v_pk_add_f32 v[36:37], v[6:7], v[64:65] op_sel_hi:[1,0] neg_lo:[0,1] neg_hi:[0,1]
	v_add_f32_e32 v0, v48, v0
	v_pk_mul_f32 v[74:75], v[36:37], v[36:37]
	v_add_f32_e32 v0, v49, v0
	v_pk_add_f32 v[34:35], v[30:31], v[64:65] op_sel_hi:[1,0] neg_lo:[0,1] neg_hi:[0,1]
	v_add_f32_e32 v0, v74, v0
	v_pk_mul_f32 v[76:77], v[34:35], v[34:35]
	v_add_f32_e32 v0, v75, v0
	v_pk_add_f32 v[32:33], v[8:9], v[64:65] op_sel_hi:[1,0] neg_lo:[0,1] neg_hi:[0,1]
	v_add_f32_e32 v0, v76, v0
	v_pk_mul_f32 v[78:79], v[32:33], v[32:33]
	v_add_f32_e32 v0, v77, v0
	v_pk_add_f32 v[30:31], v[28:29], v[64:65] op_sel_hi:[1,0] neg_lo:[0,1] neg_hi:[0,1]
	v_add_f32_e32 v0, v78, v0
	v_pk_mul_f32 v[80:81], v[30:31], v[30:31]
	v_add_f32_e32 v0, v79, v0
	v_pk_add_f32 v[28:29], v[10:11], v[64:65] op_sel_hi:[1,0] neg_lo:[0,1] neg_hi:[0,1]
	v_add_f32_e32 v0, v80, v0
	v_pk_mul_f32 v[10:11], v[28:29], v[28:29]
	v_add_f32_e32 v0, v81, v0
	v_pk_add_f32 v[20:21], v[26:27], v[64:65] op_sel_hi:[1,0] neg_lo:[0,1] neg_hi:[0,1]
	v_add_f32_e32 v0, v10, v0
	v_pk_mul_f32 v[26:27], v[20:21], v[20:21]
	v_add_f32_e32 v0, v11, v0
	v_pk_add_f32 v[16:17], v[44:45], v[64:65] op_sel_hi:[1,0] neg_lo:[0,1] neg_hi:[0,1]
	v_add_f32_e32 v0, v26, v0
	v_pk_mul_f32 v[44:45], v[16:17], v[16:17]
	v_add_f32_e32 v0, v27, v0
	v_pk_add_f32 v[8:9], v[18:19], v[64:65] op_sel_hi:[1,0] neg_lo:[0,1] neg_hi:[0,1]
	v_add_f32_e32 v0, v44, v0
	v_pk_mul_f32 v[18:19], v[8:9], v[8:9]
	v_add_f32_e32 v0, v45, v0
	v_pk_add_f32 v[6:7], v[24:25], v[64:65] op_sel_hi:[1,0] neg_lo:[0,1] neg_hi:[0,1]
	v_add_f32_e32 v0, v18, v0
	v_pk_mul_f32 v[24:25], v[6:7], v[6:7]
	v_add_f32_e32 v0, v19, v0
	v_add_f32_e32 v0, v24, v0
	v_add_f32_e32 v0, v25, v0
	v_mov_b32_e32 v1, v105
	s_nop 0
	v_add_f32_dpp v0, v0, v0 quad_perm:[1,0,3,2] row_mask:0xf bank_mask:0xf bound_ctrl:1
	s_nop 1
	v_add_f32_dpp v0, v0, v0 quad_perm:[2,3,0,1] row_mask:0xf bank_mask:0xf bound_ctrl:1
	s_nop 1
	v_add_f32_dpp v0, v0, v0 row_half_mirror row_mask:0xf bank_mask:0xf bound_ctrl:1
	s_nop 1
	v_add_f32_dpp v0, v0, v0 row_mirror row_mask:0xf bank_mask:0xf bound_ctrl:1
	s_nop 1
	v_mov_b32_dpp v1, v0 row_bcast:15 row_mask:0xa bank_mask:0xf
	v_add_f32_e32 v0, v0, v1
	v_mov_b32_e32 v1, v105
	s_nop 1
	v_mov_b32_dpp v1, v0 row_bcast:31 row_mask:0xc bank_mask:0xf
	v_add_f32_e32 v0, v0, v1
	s_nop 0
	v_readlane_b32 s2, v0, 63
	s_nop 1
	v_fma_f32 v0, s2, v187, v183
	v_rsq_f32_e32 v10, v0
	s_mov_b64 s[2:3], -1
	v_pk_mul_f32 v[0:1], v[66:67], v[10:11] op_sel_hi:[1,0]
	v_pk_mul_f32 v[2:3], v[70:71], v[10:11] op_sel_hi:[1,0]
	v_pk_fma_f32 v[0:1], v[0:1], v[54:55], v[56:57]
	v_pk_fma_f32 v[2:3], v[2:3], v[58:59], v[60:61]
	s_cbranch_vccz .LBB0_1142
	ds_read2st64_b64 v[24:27], v62 offset0:8 offset1:16
	v_cvt_pk_bf16_f32 v4, v0, v1
	v_cvt_pk_bf16_f32 v5, v2, v3
	global_store_dwordx2 v[14:15], v[4:5], off
	s_mov_b64 s[2:3], 0
	s_waitcnt lgkmcnt(0)
	v_lshlrev_b32_e32 v18, 16, v26
	v_and_b32_e32 v19, 0xffff0000, v26
	v_lshlrev_b32_e32 v4, 16, v24
	v_and_b32_e32 v5, 0xffff0000, v24
	v_pk_add_f32 v[18:19], v[18:19], 1.0 op_sel_hi:[1,0]
	v_lshlrev_b32_e32 v24, 16, v27
	v_pk_fma_f32 v[4:5], v[0:1], v[18:19], v[4:5]
	v_lshlrev_b32_e32 v18, 16, v25
	v_and_b32_e32 v19, 0xffff0000, v25
	v_and_b32_e32 v25, 0xffff0000, v27
	v_pk_add_f32 v[24:25], v[24:25], 1.0 op_sel_hi:[1,0]
	v_cvt_pk_bf16_f32 v4, v4, v5
	v_pk_fma_f32 v[18:19], v[2:3], v[24:25], v[18:19]
	s_nop 0
	v_cvt_pk_bf16_f32 v5, v18, v19
